# SCAN1: row total = prefix at lane 15 via row_newbcast (drops 2nd DPP butterfly), G=exp(total) taken from ep lane 15 (16 exec-masked exp blocks removed), f16x4(-acc) via 2 cvt_pk with neg modifiers ins
# speedup vs baseline: 1.0051x; 1.0051x over previous
.LBB0_1289:
	s_or_b64 exec, exec, s[0:1]
	v_lshlrev_b32_e32 v214, 3, v212
	s_waitcnt lgkmcnt(0)
	v_add_u32_e32 v216, s36, v214
	v_add_u32_e32 v130, 0x3c00, v216
	ds_read_b64_tr_b16 v[132:133], v130
	v_add_u32_e32 v130, 0x3e00, v216
	ds_read_b64_tr_b16 v[170:171], v130
	v_add_u32_e32 v130, 0x800, v216
	ds_read_b64_tr_b16 v[148:149], v130
	v_add_u32_e32 v130, 0xa00, v216
	ds_read_b64_tr_b16 v[150:151], v130
	v_add_u32_e32 v130, 0x3000, v216
	ds_read_b64_tr_b16 v[136:137], v216
	ds_read_b64_tr_b16 v[142:143], v130
	v_add_u32_e32 v130, 0x200, v216
	ds_read_b64_tr_b16 v[140:141], v130
	v_add_u32_e32 v130, 0x3200, v216
	ds_read_b64_tr_b16 v[138:139], v130
	v_add_u32_e32 v130, 0x400, v216
	ds_read_b64_tr_b16 v[172:173], v130
	v_add_u32_e32 v130, 0x3400, v216
	ds_read_b64_tr_b16 v[134:135], v130
	v_add_u32_e32 v130, 0x600, v216
	ds_read_b64_tr_b16 v[174:175], v130
	v_add_u32_e32 v130, 0x3600, v216
	ds_read_b64_tr_b16 v[130:131], v130
	s_waitcnt lgkmcnt(0)
	v_mfma_f32_16x16x16_f16 v[156:159], v[170:171], v[142:143], 0
	v_mfma_f32_16x16x16_f16 v[152:155], v[132:133], v[136:137], 0
	v_mfma_f32_16x16x16_f16 v[166:169], v[170:171], v[138:139], 0
	s_nop 5
	v_cvt_pk_f16_f32 v137, v158, v159
	v_cvt_pk_f16_f32 v136, v156, v157
	v_cvt_pk_f16_f32 v203, v154, v155
	v_cvt_pk_f16_f32 v202, v152, v153
	v_mfma_f32_16x16x16_f16 v[156:159], v[132:133], v[136:137], 0
	v_cvt_pk_f16_f32 v137, v168, v169
	v_cvt_pk_f16_f32 v136, v166, v167
	v_mfma_f32_16x16x16_f16 v[152:155], v[132:133], v[172:173], 0
	s_nop 0
	v_mfma_f32_16x16x16_f16 v[166:169], v[132:133], v[136:137], 0
	s_nop 2
	v_cvt_pk_f16_f32 v147, v158, v159
	v_cvt_pk_f16_f32 v146, v156, v157
	s_nop 0
	v_cvt_pk_f16_f32 v199, v154, v155
	v_mfma_f32_16x16x16_f16 v[156:159], v[170:171], v[134:135], 0
	v_cvt_pk_f16_f32 v198, v152, v153
	v_mfma_f32_16x16x16_f16 v[152:155], v[132:133], v[174:175], 0
	v_mfma_f32_16x16x16_f16 v[162:165], v[132:133], v[140:141], 0
	s_nop 4
	v_cvt_pk_f16_f32 v137, v158, v159
	v_cvt_pk_f16_f32 v136, v156, v157
	v_cvt_pk_f16_f32 v197, v154, v155
	v_cvt_pk_f16_f32 v196, v152, v153
	v_mfma_f32_16x16x16_f16 v[156:159], v[132:133], v[136:137], 0
	v_cvt_pk_f16_f32 v200, v162, v163
	v_cvt_pk_f16_f32 v201, v164, v165
	v_cvt_pk_f16_f32 v141, v168, v169
	v_cvt_pk_f16_f32 v140, v166, v167
	s_nop 3
	v_cvt_pk_f16_f32 v136, v156, v157
	v_mfma_f32_16x16x16_f16 v[154:157], v[170:171], v[130:131], 0
	v_cvt_pk_f16_f32 v137, v158, v159
	s_nop 6
	v_cvt_pk_f16_f32 v153, v156, v157
	v_cvt_pk_f16_f32 v152, v154, v155
	s_nop 1
	v_mfma_f32_16x16x16_f16 v[152:155], v[132:133], v[152:153], 0
	s_nop 7
	v_cvt_pk_f16_f32 v132, v152, v153
	v_add_u32_e32 v152, 0x1800, v216
	ds_read_b64_tr_b16 v[156:157], v152
	v_add_u32_e32 v152, 0x1a00, v216
	ds_read_b64_tr_b16 v[158:159], v152
	v_add_u32_e32 v152, 0x1c00, v216
	ds_read_b64_tr_b16 v[162:163], v152
	v_add_u32_e32 v152, 0x1e00, v216
	ds_read_b64_tr_b16 v[164:165], v152
	s_waitcnt lgkmcnt(0)
	v_cvt_pk_f16_f32 v133, v154, v155
	v_cvt_f32_f16_sdwa v161, v156 dst_sel:DWORD dst_unused:UNUSED_PAD src0_sel:WORD_1
	v_cvt_f32_f16_e32 v156, v156
	v_mfma_f32_16x16x16_f16 v[152:155], v[148:149], v[202:203], 0
	v_cvt_f32_f16_e32 v166, v157
	v_cvt_f32_f16_sdwa v157, v157 dst_sel:DWORD dst_unused:UNUSED_PAD src0_sel:WORD_1
	s_nop 5
	v_sub_f32_e32 v152, v156, v152
	v_sub_f32_e32 v153, v161, v153
	v_sub_f32_e32 v154, v166, v154
	v_sub_f32_e32 v155, v157, v155
	v_cvt_pk_f16_f32 v157, v154, v155
	v_cvt_pk_f16_f32 v156, v152, v153
	v_mfma_f32_16x16x16_f16 v[152:155], v[148:149], v[200:201], 0
	v_cvt_f32_f16_e32 v161, v158
	v_cvt_f32_f16_sdwa v158, v158 dst_sel:DWORD dst_unused:UNUSED_PAD src0_sel:WORD_1
	v_cvt_f32_f16_e32 v166, v159
	v_cvt_f32_f16_sdwa v159, v159 dst_sel:DWORD dst_unused:UNUSED_PAD src0_sel:WORD_1
	s_nop 3
	v_sub_f32_e32 v152, v161, v152
	v_sub_f32_e32 v158, v158, v153
	v_sub_f32_e32 v153, v166, v154
	v_sub_f32_e32 v154, v159, v155
	v_cvt_pk_f16_f32 v153, v153, v154
	v_cvt_pk_f16_f32 v152, v152, v158
	ds_write2st64_b64 v160, v[156:157], v[152:153] offset0:8 offset1:9
	v_mfma_f32_16x16x16_f16 v[152:155], v[148:149], v[198:199], 0
	v_cvt_f32_f16_e32 v156, v162
	v_cvt_f32_f16_sdwa v157, v162 dst_sel:DWORD dst_unused:UNUSED_PAD src0_sel:WORD_1
	v_cvt_f32_f16_e32 v158, v163
	v_cvt_f32_f16_sdwa v159, v163 dst_sel:DWORD dst_unused:UNUSED_PAD src0_sel:WORD_1
	v_cvt_f32_f16_e32 v161, v165
	s_nop 2
	v_sub_f32_e32 v152, v156, v152
	v_sub_f32_e32 v153, v157, v153
	v_sub_f32_e32 v154, v158, v154
	v_sub_f32_e32 v155, v159, v155
	v_cvt_pk_f16_f32 v157, v154, v155
	v_cvt_pk_f16_f32 v156, v152, v153
	v_mfma_f32_16x16x16_f16 v[152:155], v[148:149], v[196:197], 0
	v_cvt_f32_f16_e32 v158, v164
	v_cvt_f32_f16_sdwa v159, v164 dst_sel:DWORD dst_unused:UNUSED_PAD src0_sel:WORD_1
	v_cvt_f32_f16_sdwa v162, v165 dst_sel:DWORD dst_unused:UNUSED_PAD src0_sel:WORD_1
	s_nop 4
	v_sub_f32_e32 v152, v158, v152
	v_sub_f32_e32 v158, v159, v153
	v_sub_f32_e32 v153, v161, v154
	v_sub_f32_e32 v154, v162, v155
	v_cvt_pk_f16_f32 v153, v153, v154
	v_cvt_pk_f16_f32 v152, v152, v158
	ds_write2st64_b64 v160, v[156:157], v[152:153] offset0:10 offset1:11
	s_waitcnt lgkmcnt(0)
	v_add_u32_e32 v152, 0x1000, v216
	ds_read_b64_tr_b16 v[152:153], v152
	v_add_u32_e32 v154, 0x1200, v216
	ds_read_b64_tr_b16 v[158:159], v154
	v_add_u32_e32 v154, 0x1400, v216
	ds_read_b64_tr_b16 v[206:207], v154
	v_add_u32_e32 v154, 0x1600, v216
	ds_read_b64_tr_b16 v[204:205], v154
	s_waitcnt lgkmcnt(0)
	v_cvt_pk_f16_f32 v183, v4, v5
	v_cvt_pk_f16_f32 v182, v2, v3
	v_mfma_f32_16x16x16_f16 v[154:157], v[150:151], v[142:143], 0
	v_cvt_pk_f16_f32 v189, v44, v45
	v_cvt_pk_f16_f32 v188, v42, v43
	v_cvt_pk_f16_f32 v187, v8, v9
	v_mfma_f32_16x16x16_f16 v[160:163], v[148:149], v[146:147], 0
	v_cvt_pk_f16_f32 v186, v6, v7
	v_cvt_pk_f16_f32 v193, v68, v69
	v_cvt_pk_f16_f32 v192, v66, v67
	v_mfma_f32_16x16x16_f16 v[2:5], v[152:153], v[182:183], 0
	v_cvt_pk_f16_f32 v191, v12, v13
	s_nop 2
	v_sub_f32_e32 v157, v157, v163
	v_sub_f32_e32 v156, v156, v162
	v_sub_f32_e32 v155, v155, v161
	v_sub_f32_e32 v154, v154, v160
	v_mfma_f32_16x16x16_f16 v[2:5], v[158:159], v[188:189], v[2:5]
	v_cvt_pk_f16_f32 v190, v10, v11
	v_cvt_pk_f16_f32 v81, v80, v81
	v_cvt_pk_f16_f32 v80, v78, v79
	v_mfma_f32_16x16x16_f16 v[6:9], v[152:153], v[186:187], v[154:157]
	v_cvt_pk_f16_f32 v195, v16, v17
	v_cvt_pk_f16_f32 v194, v14, v15
	v_cvt_pk_f16_f32 v41, v40, v41
	v_mfma_f32_16x16x16_f16 v[2:5], v[206:207], v[192:193], v[2:5]
	v_cvt_pk_f16_f32 v40, v38, v39
	v_lshlrev_b32_e32 v10, 1, v144
	v_add3_u32 v38, s36, v10, v178
	v_mfma_f32_16x16x16_f16 v[6:9], v[158:159], v[190:191], v[6:9]
	v_cvt_pk_f16_f32 v167, v92, v93
	v_cvt_pk_f16_f32 v166, v90, v91
	v_cvt_pk_f16_f32 v169, v28, v29
	v_mfma_f32_16x16x16_f16 v[2:5], v[204:205], v[80:81], v[2:5]
	v_cvt_pk_f16_f32 v168, v26, v27
	v_cvt_pk_f16_f32 v173, v76, v77
	v_cvt_pk_f16_f32 v172, v74, v75
	v_mfma_f32_16x16x16_f16 v[6:9], v[206:207], v[194:195], v[6:9]
	v_cvt_pk_f16_f32 v177, v20, v21
	s_nop 2
	v_cvt_f16_f32_e32 v2, v2
	v_cvt_f16_f32_e32 v4, v4
	v_mfma_f32_16x16x16_f16 v[6:9], v[204:205], v[40:41], v[6:9]
	v_cvt_pk_f16_f32 v176, v18, v19
	ds_write_b16 v38, v2
	v_cvt_f16_f32_e32 v2, v3
	v_mfma_f32_16x16x16_f16 v[10:13], v[150:151], v[138:139], 0
	v_cvt_pk_f16_f32 v181, v84, v85
	s_nop 2
	v_cvt_f16_f32_e32 v6, v6
	v_cvt_f16_f32_e32 v3, v7
	v_mfma_f32_16x16x16_f16 v[14:17], v[148:149], v[140:141], 0
	ds_write_b16 v38, v2 offset:128
	v_cvt_f16_f32_e32 v2, v8
	ds_write_b16 v38, v6 offset:6144
	v_mfma_f32_16x16x16_f16 v[42:45], v[152:153], v[166:167], 0
	v_cvt_f16_f32_e32 v6, v5
	s_nop 2
	v_sub_f32_e32 v13, v13, v17
	v_sub_f32_e32 v12, v12, v16
	v_sub_f32_e32 v11, v11, v15
	v_sub_f32_e32 v10, v10, v14
	v_mfma_f32_16x16x16_f16 v[14:17], v[158:159], v[172:173], v[42:45]
	ds_write_b16 v38, v3 offset:6272
	ds_write_b16 v38, v4 offset:256
	ds_write_b16 v38, v2 offset:6400
	v_cvt_pk_f16_f32 v180, v82, v83
	v_mfma_f32_16x16x16_f16 v[10:13], v[152:153], v[168:169], v[10:13]
	ds_write_b16 v38, v6 offset:384
	v_cvt_f16_f32_e32 v6, v9
	v_cvt_pk_f16_f32 v185, v24, v25
	v_mfma_f32_16x16x16_f16 v[2:5], v[158:159], v[176:177], v[10:13]
	v_cvt_pk_f16_f32 v184, v22, v23
	v_cvt_pk_f16_f32 v89, v88, v89
	v_cvt_pk_f16_f32 v88, v86, v87
	v_mfma_f32_16x16x16_f16 v[10:13], v[206:207], v[180:181], v[14:17]
	ds_write_b16 v38, v6 offset:6528
	v_cvt_pk_f16_f32 v33, v32, v33
	v_cvt_pk_f16_f32 v32, v30, v31
	v_mfma_f32_16x16x16_f16 v[2:5], v[206:207], v[184:185], v[2:5]
	v_cvt_pk_f16_f32 v161, v112, v113
	v_cvt_pk_f16_f32 v160, v110, v111
	v_cvt_pk_f16_f32 v163, v60, v61
	v_mfma_f32_16x16x16_f16 v[6:9], v[204:205], v[88:89], v[10:13]
	v_cvt_pk_f16_f32 v162, v58, v59
	v_cvt_pk_f16_f32 v165, v96, v97
	v_cvt_pk_f16_f32 v164, v94, v95
	v_mfma_f32_16x16x16_f16 v[10:13], v[150:151], v[134:135], 0
	v_cvt_pk_f16_f32 v171, v36, v37
	s_nop 2
	v_cvt_f16_f32_e32 v6, v6
	v_cvt_pk_f16_f32 v170, v34, v35
	v_mfma_f32_16x16x16_f16 v[14:17], v[148:149], v[136:137], 0
	v_cvt_pk_f16_f32 v175, v104, v105
	ds_write_b16 v38, v6 offset:32
	v_cvt_f16_f32_e32 v6, v7
	v_mfma_f32_16x16x16_f16 v[2:5], v[204:205], v[32:33], v[2:5]
	v_cvt_pk_f16_f32 v174, v102, v103
	s_nop 2
	v_sub_f32_e32 v13, v13, v17
	v_sub_f32_e32 v12, v12, v16
	v_sub_f32_e32 v11, v11, v15
	v_mfma_f32_16x16x16_f16 v[16:19], v[152:153], v[160:161], 0
	v_sub_f32_e32 v10, v10, v14
	v_cvt_f16_f32_e32 v2, v2
	v_cvt_f16_f32_e32 v3, v3
	v_mfma_f32_16x16x16_f16 v[10:13], v[152:153], v[162:163], v[10:13]
	ds_write_b16 v38, v2 offset:6176
	ds_write_b16 v38, v6 offset:160
	ds_write_b16 v38, v3 offset:6304
	v_cvt_f16_f32_e32 v2, v8
	v_mfma_f32_16x16x16_f16 v[14:17], v[158:159], v[164:165], v[16:19]
	v_cvt_pk_f16_f32 v179, v52, v53
	v_cvt_pk_f16_f32 v178, v50, v51
	ds_write_b16 v38, v2 offset:288
	v_mfma_f32_16x16x16_f16 v[10:13], v[158:159], v[170:171], v[10:13]
	v_cvt_f16_f32_e32 v2, v4
	v_cvt_pk_f16_f32 v109, v108, v109
	v_cvt_pk_f16_f32 v108, v106, v107
	v_mfma_f32_16x16x16_f16 v[14:17], v[206:207], v[174:175], v[14:17]
	v_cvt_f16_f32_e32 v18, v9
	v_cvt_pk_f16_f32 v57, v56, v57
	v_cvt_pk_f16_f32 v56, v54, v55
	v_mfma_f32_16x16x16_f16 v[10:13], v[206:207], v[178:179], v[10:13]
	ds_write_b16 v38, v2 offset:6432
	v_cvt_pk_f16_f32 v157, v116, v117
	v_cvt_pk_f16_f32 v156, v114, v115
	v_mfma_f32_16x16x16_f16 v[6:9], v[204:205], v[108:109], v[14:17]
	v_cvt_pk_f16_f32 v155, v100, v101
	v_cvt_pk_f16_f32 v154, v98, v99
	v_cvt_pk_f16_f32 v125, v124, v125
	v_cvt_f16_f32_e32 v14, v5
	v_mfma_f32_16x16x16_f16 v[2:5], v[204:205], v[56:57], v[10:13]
	s_nop 2
	v_cvt_f16_f32_e32 v6, v6
	v_cvt_pk_f16_f32 v124, v122, v123
	v_cvt_pk_f16_f32 v129, v128, v129
	v_mfma_f32_16x16x16_f16 v[10:13], v[150:151], v[130:131], 0
	v_cvt_pk_f16_f32 v151, v72, v73
	v_cvt_f16_f32_e32 v2, v2
	ds_write_b16 v38, v18 offset:416
	ds_write_b16 v38, v14 offset:6560
	ds_write_b16 v38, v6 offset:64
	ds_write_b16 v38, v2 offset:6208
	v_mfma_f32_16x16x16_f16 v[14:17], v[148:149], v[132:133], 0
	v_cvt_f16_f32_e32 v2, v7
	v_cvt_pk_f16_f32 v149, v64, v65
	v_cvt_pk_f16_f32 v148, v62, v63
	v_cvt_f16_f32_e32 v3, v3
	v_cvt_f16_f32_e32 v6, v8
	s_nop 2
	v_sub_f32_e32 v13, v13, v17
	v_sub_f32_e32 v12, v12, v16
	v_sub_f32_e32 v11, v11, v15
	v_mfma_f32_16x16x16_f16 v[16:19], v[152:153], v[156:157], 0
	v_sub_f32_e32 v10, v10, v14
	ds_write_b16 v38, v2 offset:192
	ds_write_b16 v38, v3 offset:6336
	ds_write_b16 v38, v6 offset:320
	v_cvt_f16_f32_e32 v2, v4
	v_mfma_f32_16x16x16_f16 v[10:13], v[152:153], v[148:149], v[10:13]
	v_cvt_pk_f16_f32 v153, v48, v49
	v_cvt_pk_f16_f32 v152, v46, v47
	ds_write_b16 v38, v2 offset:6464
	v_mfma_f32_16x16x16_f16 v[14:17], v[158:159], v[154:155], v[16:19]
	v_cvt_f16_f32_e32 v2, v9
	v_cvt_pk_f16_f32 v150, v70, v71
	v_cvt_pk_f16_f32 v128, v126, v127
	v_mfma_f32_16x16x16_f16 v[10:13], v[158:159], v[152:153], v[10:13]
	v_cvt_pk_f16_f32 v159, v120, v121
	v_cvt_pk_f16_f32 v158, v118, v119
	ds_write_b16 v38, v2 offset:448
	v_mfma_f32_16x16x16_f16 v[10:13], v[206:207], v[150:151], v[10:13]
	v_mfma_f32_16x16x16_f16 v[6:9], v[206:207], v[158:159], v[14:17]
	s_nop 2
	v_cvt_f16_f32_e32 v14, v5
	v_mfma_f32_16x16x16_f16 v[2:5], v[204:205], v[124:125], v[6:9]
	ds_write_b16 v38, v14 offset:6592
	v_mfma_f32_16x16x16_f16 v[6:9], v[204:205], v[128:129], v[10:13]
	s_nop 5
	v_cvt_f16_f32_e32 v2, v2
	s_nop 0
	v_cvt_f16_f32_e32 v6, v6
	v_cvt_f16_f32_e32 v3, v3
	v_cvt_f16_f32_e32 v7, v7
	ds_write_b16 v38, v2 offset:96
	ds_write_b16 v38, v6 offset:6240
	ds_write_b16 v38, v3 offset:224
	ds_write_b16 v38, v7 offset:6368
	v_cvt_f16_f32_e32 v2, v4
	v_cvt_f16_f32_e32 v3, v8
	v_cvt_f16_f32_e32 v4, v5
	v_cvt_f16_f32_e32 v5, v9
	ds_write_b16 v38, v2 offset:352
	ds_write_b16 v38, v3 offset:6496
	ds_write_b16 v38, v4 offset:480
	ds_write_b16 v38, v5 offset:6624
	v_add_u32_e32 v2, 0x2000, v216
	ds_read_b64_tr_b16 v[62:63], v2
	v_add_u32_e32 v3, 0x2800, v216
	ds_read_b64_tr_b16 v[64:65], v3
	v_add_u32_e32 v2, 0x2200, v216
	ds_read_b64_tr_b16 v[46:47], v2
	v_add_u32_e32 v2, 0x2a00, v216
	ds_read_b64_tr_b16 v[48:49], v2
	v_add_u32_e32 v2, 0x2400, v216
	ds_read_b64_tr_b16 v[118:119], v2
	v_add_u32_e32 v2, 0x2c00, v216
	ds_read_b64_tr_b16 v[120:121], v2
	v_add_u32_e32 v2, 0x2600, v216
	ds_read_b64_tr_b16 v[70:71], v2
	v_add_u32_e32 v2, 0x2e00, v216
	ds_read_b64_tr_b16 v[72:73], v2
	v_add_u32_e32 v2, 0x4000, v215
	ds_read2_b32 v[10:11], v2 offset1:16
	ds_read2_b32 v[18:19], v2 offset0:32 offset1:48
	s_waitcnt lgkmcnt(0)
	v_mfma_f32_16x16x16_f16 v[2:5], v[202:203], v[62:63], 0
	v_cmp_eq_u32_e32 vcc, v208, v144
	v_cmp_eq_u32_e64 s[0:1], v211, v144
	v_cmp_eq_u32_e64 s[2:3], v209, v144
	v_mfma_f32_16x16x16_f16 v[6:9], v[202:203], v[46:47], 0
	s_waitcnt lgkmcnt(1)
	v_cndmask_b32_e32 v12, 0, v10, vcc
	s_nop 1
	v_sub_f32_e32 v2, v12, v2
	v_cndmask_b32_e64 v12, 0, v10, s[0:1]
	v_mfma_f32_16x16x16_f16 v[24:27], v[202:203], v[70:71], 0
	v_cmp_eq_u32_e64 s[4:5], v210, v144
	v_sub_f32_e32 v3, v12, v3
	v_cndmask_b32_e64 v12, 0, v10, s[2:3]
	v_cndmask_b32_e64 v10, 0, v10, s[4:5]
	v_mfma_f32_16x16x16_f16 v[20:23], v[202:203], v[118:119], 0
	v_sub_f32_e32 v5, v10, v5
	v_cvt_pk_f16_f32 v98, v2, v3

	v_mfma_f32_16x16x16_f16 v[28:31], v[200:201], v[62:63], 0


	v_sub_f32_e32 v4, v12, v4


	v_cvt_pk_f16_f32 v99, v4, v5
	v_mfma_f32_16x16x16_f16 v[2:5], v[198:199], v[62:63], 0
	v_cvt_pk_f16_f32 v100, -v6, -v7
	v_cvt_pk_f16_f32 v101, -v8, -v9


	v_cvt_pk_f16_f32 v122, -v24, -v25


	s_nop 0
	v_cvt_pk_f16_f32 v115, -v30, -v31
	v_cvt_pk_f16_f32 v114, -v28, -v29
	v_mfma_f32_16x16x16_f16 v[28:31], v[64:65], v[142:143], 0


	v_mfma_f32_16x16x16_f16 v[82:85], v[62:63], v[146:147], 0


	v_cvt_pk_f16_f32 v126, -v20, -v21
	v_cvt_pk_f16_f32 v127, -v22, -v23
	v_mfma_f32_16x16x16_f16 v[6:9], v[196:197], v[62:63], 0


	s_nop 3
	v_sub_f32_e32 v31, v31, v85
	v_sub_f32_e32 v30, v30, v84
	v_sub_f32_e32 v29, v29, v83
	v_sub_f32_e32 v28, v28, v82


	s_nop 0
	v_mfma_f32_16x16x16_f16 v[28:31], v[98:99], v[186:187], v[28:31]


	v_cvt_pk_f16_f32 v116, -v2, -v3
	v_cvt_pk_f16_f32 v117, -v4, -v5

	v_mfma_f32_16x16x16_f16 v[34:37], v[200:201], v[46:47], 0


	s_nop 3
	v_mfma_f32_16x16x16_f16 v[28:31], v[114:115], v[190:191], v[28:31]


	v_cvt_pk_f16_f32 v123, -v26, -v27

	v_mfma_f32_16x16x16_f16 v[42:45], v[198:199], v[46:47], 0
	s_waitcnt lgkmcnt(0)
	v_add_u32_e32 v144, s36, v213
	s_add_u32 s26, s26, 16
	v_mfma_f32_16x16x16_f16 v[58:61], v[198:199], v[118:119], 0
	s_addc_u32 s27, s27, 0
	s_nop 3

	s_cmpk_eq_i32 s26, 0x100
	v_mfma_f32_16x16x16_f16 v[20:23], v[198:199], v[70:71], 0
	s_nop 6
	v_cvt_pk_f16_f32 v198, -v6, -v7
	v_cndmask_b32_e32 v10, 0, v11, vcc
	v_cvt_pk_f16_f32 v199, -v8, -v9
	v_mfma_f32_16x16x16_f16 v[6:9], v[116:117], v[194:195], v[28:31]
	s_nop 2
	v_sub_f32_e32 v28, v10, v34
	v_cndmask_b32_e64 v10, 0, v11, s[0:1]
	v_sub_f32_e32 v29, v10, v35
	v_cndmask_b32_e64 v10, 0, v11, s[2:3]
	v_cndmask_b32_e64 v11, 0, v11, s[4:5]
	v_sub_f32_e32 v10, v10, v36
	v_sub_f32_e32 v11, v11, v37
	v_mfma_f32_16x16x16_f16 v[66:69], v[196:197], v[46:47], 0


	v_mfma_f32_16x16x16_f16 v[24:27], v[196:197], v[118:119], 0


	v_cvt_pk_f16_f32 v202, -v42, -v43
	v_mfma_f32_16x16x16_f16 v[74:77], v[196:197], v[70:71], 0
	s_nop 3
	v_cvt_pk_f16_f32 v197, v10, v11
	v_cvt_pk_f16_f32 v196, v28, v29
	v_cvt_pk_f16_f32 v203, -v44, -v45
	v_mfma_f32_16x16x16_f16 v[10:13], v[48:49], v[142:143], 0
	v_mfma_f32_16x16x16_f16 v[28:31], v[46:47], v[146:147], 0
	v_mfma_f32_16x16x16_f16 v[34:37], v[100:101], v[182:183], 0
	v_mfma_f32_16x16x16_f16 v[50:53], v[200:201], v[118:119], 0
	s_nop 5
	v_sub_f32_e32 v13, v13, v31
	v_sub_f32_e32 v12, v12, v30
	v_sub_f32_e32 v11, v11, v29
	v_sub_f32_e32 v10, v10, v28
	v_mfma_f32_16x16x16_f16 v[28:31], v[196:197], v[188:189], v[34:37]
	s_nop 2


	s_nop 3
	v_mfma_f32_16x16x16_f16 v[28:31], v[202:203], v[192:193], v[28:31]

	v_cvt_pk_f16_f32 v210, -v66, -v67
	v_cvt_pk_f16_f32 v211, -v68, -v69


	s_nop 2
	v_mfma_f32_16x16x16_f16 v[42:45], v[210:211], v[80:81], v[28:31]

	s_nop 1


	s_waitcnt lgkmcnt(0)
	v_cndmask_b32_e32 v34, 0, v18, vcc

	v_cvt_pk_f16_f32 v206, -v50, -v51
	v_cvt_pk_f16_f32 v207, -v52, -v53
	v_sub_f32_e32 v38, v34, v58
	v_cndmask_b32_e64 v34, 0, v18, s[0:1]
	v_cndmask_b32_e64 v50, 0, v18, s[2:3]
	v_mfma_f32_16x16x16_f16 v[28:31], v[120:121], v[142:143], 0
	v_sub_f32_e32 v39, v34, v59
	v_sub_f32_e32 v58, v50, v60
	v_cndmask_b32_e64 v18, 0, v18, s[4:5]
	v_mfma_f32_16x16x16_f16 v[34:37], v[118:119], v[146:147], 0
	v_sub_f32_e32 v18, v18, v61
	v_cvt_pk_f16_f32 v205, v58, v18
	v_cvt_pk_f16_f32 v204, v38, v39
	v_mfma_f32_16x16x16_f16 v[50:53], v[126:127], v[182:183], 0

	s_nop 2
	v_sub_f32_e32 v31, v31, v37
	v_sub_f32_e32 v30, v30, v36
	v_sub_f32_e32 v29, v29, v35
	v_sub_f32_e32 v28, v28, v34
	v_mfma_f32_16x16x16_f16 v[34:37], v[206:207], v[188:189], v[50:53]


	v_mfma_f32_16x16x16_f16 v[28:31], v[126:127], v[186:187], v[28:31]
	v_cvt_pk_f16_f32 v209, -v26, -v27
	v_cvt_pk_f16_f32 v208, -v24, -v25
	s_nop 2
	v_mfma_f32_16x16x16_f16 v[24:27], v[204:205], v[192:193], v[34:37]
	s_nop 2


	v_mfma_f32_16x16x16_f16 v[14:17], v[200:201], v[70:71], 0

	v_mfma_f32_16x16x16_f16 v[28:31], v[206:207], v[190:191], v[28:31]
	v_mfma_f32_16x16x16_f16 v[28:31], v[204:205], v[194:195], v[28:31]
	s_nop 4


	v_mfma_f32_16x16x16_f16 v[66:69], v[208:209], v[80:81], v[24:27]
	s_nop 2


	v_cvt_pk_f16_f32 v201, -v16, -v17
	v_cvt_pk_f16_f32 v200, -v14, -v15
	v_mfma_f32_16x16x16_f16 v[14:17], v[208:209], v[40:41], v[28:31]


	s_nop 0
	v_mfma_f32_16x16x16_f16 v[24:27], v[72:73], v[142:143], 0


	s_nop 4
	v_mfma_f32_16x16x16_f16 v[28:31], v[70:71], v[146:147], 0


	v_mfma_f32_16x16x16_f16 v[90:93], v[98:99], v[182:183], 0
	v_mfma_f32_16x16x16_f16 v[10:13], v[100:101], v[186:187], v[10:13]
	s_nop 3
	s_nop 0
	v_cvt_pk_f16_f32 v147, -v22, -v23
	v_sub_f32_e32 v23, v27, v31
	v_sub_f32_e32 v22, v26, v30
	v_cvt_pk_f16_f32 v146, -v20, -v21
	v_sub_f32_e32 v21, v25, v29
	v_sub_f32_e32 v20, v24, v28
	v_mfma_f32_16x16x16_f16 v[34:37], v[122:123], v[182:183], 0


	v_mfma_f32_16x16x16_f16 v[20:23], v[122:123], v[186:187], v[20:23]
	v_cndmask_b32_e32 v18, 0, v19, vcc
	v_sub_f32_e32 v28, v18, v74
	v_cndmask_b32_e64 v18, 0, v19, s[0:1]
	v_mfma_f32_16x16x16_f16 v[2:5], v[114:115], v[188:189], v[90:93]
	v_sub_f32_e32 v29, v18, v75
	v_cndmask_b32_e64 v18, 0, v19, s[2:3]
	v_cndmask_b32_e64 v19, 0, v19, s[4:5]
	v_mfma_f32_16x16x16_f16 v[10:13], v[196:197], v[190:191], v[10:13]
	v_sub_f32_e32 v18, v18, v76
	v_sub_f32_e32 v19, v19, v77
	v_cvt_pk_f16_f32 v143, v18, v19
	v_mfma_f32_16x16x16_f16 v[24:27], v[200:201], v[188:189], v[34:37]
	v_cvt_pk_f16_f32 v142, v28, v29
	v_mfma_f32_16x16x16_f16 v[20:23], v[200:201], v[190:191], v[20:23]
	v_mfma_f32_16x16x16_f16 v[2:5], v[116:117], v[192:193], v[2:5]
	v_mfma_f32_16x16x16_f16 v[10:13], v[202:203], v[194:195], v[10:13]
	v_mfma_f32_16x16x16_f16 v[24:27], v[146:147], v[192:193], v[24:27]
	v_mfma_f32_16x16x16_f16 v[18:21], v[146:147], v[194:195], v[20:23]
	v_mfma_f32_16x16x16_f16 v[2:5], v[198:199], v[80:81], v[2:5]
	v_mfma_f32_16x16x16_f16 v[6:9], v[198:199], v[40:41], v[6:9]
	v_mfma_f32_16x16x16_f16 v[10:13], v[210:211], v[40:41], v[10:13]
	v_mfma_f32_16x16x16_f16 v[78:81], v[142:143], v[80:81], v[24:27]
	v_mfma_f32_16x16x16_f16 v[38:41], v[142:143], v[40:41], v[18:21]
	v_mfma_f32_16x16x16_f16 v[18:21], v[64:65], v[138:139], 0
	v_mfma_f32_16x16x16_f16 v[22:25], v[62:63], v[140:141], 0
	v_mfma_f32_16x16x16_f16 v[26:29], v[98:99], v[166:167], 0
	v_mfma_f32_16x16x16_f16 v[34:37], v[100:101], v[166:167], 0
	s_nop 5
	v_sub_f32_e32 v21, v21, v25
	v_sub_f32_e32 v20, v20, v24
	v_sub_f32_e32 v19, v19, v23
	v_sub_f32_e32 v18, v18, v22
	v_mfma_f32_16x16x16_f16 v[22:25], v[114:115], v[172:173], v[26:29]
	s_nop 0
	v_mfma_f32_16x16x16_f16 v[18:21], v[98:99], v[168:169], v[18:21]
	v_mfma_f32_16x16x16_f16 v[18:21], v[114:115], v[176:177], v[18:21]
	v_mfma_f32_16x16x16_f16 v[22:25], v[116:117], v[180:181], v[22:25]
	v_mfma_f32_16x16x16_f16 v[18:21], v[116:117], v[184:185], v[18:21]
	v_mfma_f32_16x16x16_f16 v[90:93], v[198:199], v[88:89], v[22:25]
	v_mfma_f32_16x16x16_f16 v[26:29], v[198:199], v[32:33], v[18:21]
	v_mfma_f32_16x16x16_f16 v[18:21], v[48:49], v[138:139], 0
	v_mfma_f32_16x16x16_f16 v[22:25], v[46:47], v[140:141], 0
	v_mfma_f32_16x16x16_f16 v[50:53], v[126:127], v[166:167], 0
	v_mfma_f32_16x16x16_f16 v[58:61], v[122:123], v[166:167], 0
	s_nop 5
	v_sub_f32_e32 v21, v21, v25
	v_sub_f32_e32 v20, v20, v24
	v_sub_f32_e32 v19, v19, v23
	v_sub_f32_e32 v18, v18, v22
	v_mfma_f32_16x16x16_f16 v[22:25], v[196:197], v[172:173], v[34:37]
	v_mfma_f32_16x16x16_f16 v[22:25], v[202:203], v[180:181], v[22:25]
	v_mfma_f32_16x16x16_f16 v[74:77], v[210:211], v[88:89], v[22:25]
	v_mfma_f32_16x16x16_f16 v[22:25], v[120:121], v[138:139], 0
	v_mfma_f32_16x16x16_f16 v[34:37], v[118:119], v[140:141], 0
	v_mfma_f32_16x16x16_f16 v[18:21], v[100:101], v[168:169], v[18:21]
	v_mfma_f32_16x16x16_f16 v[18:21], v[196:197], v[176:177], v[18:21]
	s_nop 5
	v_sub_f32_e32 v25, v25, v37
	v_sub_f32_e32 v24, v24, v36
	v_sub_f32_e32 v23, v23, v35
	v_sub_f32_e32 v22, v22, v34
	v_mfma_f32_16x16x16_f16 v[34:37], v[206:207], v[172:173], v[50:53]
	v_mfma_f32_16x16x16_f16 v[34:37], v[204:205], v[180:181], v[34:37]
	v_mfma_f32_16x16x16_f16 v[82:85], v[208:209], v[88:89], v[34:37]
	v_mfma_f32_16x16x16_f16 v[34:37], v[72:73], v[138:139], 0
	v_mfma_f32_16x16x16_f16 v[50:53], v[70:71], v[140:141], 0
	v_mfma_f32_16x16x16_f16 v[22:25], v[126:127], v[168:169], v[22:25]
	v_mfma_f32_16x16x16_f16 v[22:25], v[206:207], v[176:177], v[22:25]
	s_nop 5
	v_sub_f32_e32 v37, v37, v53
	v_sub_f32_e32 v36, v36, v52
	v_sub_f32_e32 v35, v35, v51
	v_sub_f32_e32 v34, v34, v50
	v_mfma_f32_16x16x16_f16 v[50:53], v[200:201], v[172:173], v[58:61]
	s_nop 0
	v_mfma_f32_16x16x16_f16 v[34:37], v[122:123], v[168:169], v[34:37]
	v_mfma_f32_16x16x16_f16 v[34:37], v[200:201], v[176:177], v[34:37]
	v_mfma_f32_16x16x16_f16 v[18:21], v[202:203], v[184:185], v[18:21]
	v_mfma_f32_16x16x16_f16 v[22:25], v[204:205], v[184:185], v[22:25]
	v_mfma_f32_16x16x16_f16 v[50:53], v[146:147], v[180:181], v[50:53]
	v_mfma_f32_16x16x16_f16 v[34:37], v[146:147], v[184:185], v[34:37]
	v_mfma_f32_16x16x16_f16 v[18:21], v[210:211], v[32:33], v[18:21]
	v_mfma_f32_16x16x16_f16 v[22:25], v[208:209], v[32:33], v[22:25]
	v_mfma_f32_16x16x16_f16 v[86:89], v[142:143], v[88:89], v[50:53]
	v_mfma_f32_16x16x16_f16 v[30:33], v[142:143], v[32:33], v[34:37]
	v_mfma_f32_16x16x16_f16 v[34:37], v[64:65], v[134:135], 0
	v_mfma_f32_16x16x16_f16 v[50:53], v[62:63], v[136:137], 0
	v_mfma_f32_16x16x16_f16 v[58:61], v[98:99], v[160:161], 0
	v_mfma_f32_16x16x16_f16 v[94:97], v[100:101], v[160:161], 0
	s_nop 5
	v_sub_f32_e32 v37, v37, v53
	v_sub_f32_e32 v36, v36, v52
	v_sub_f32_e32 v35, v35, v51
	v_sub_f32_e32 v34, v34, v50
	v_mfma_f32_16x16x16_f16 v[50:53], v[114:115], v[164:165], v[58:61]
	s_nop 0
	v_mfma_f32_16x16x16_f16 v[34:37], v[98:99], v[162:163], v[34:37]
	v_mfma_f32_16x16x16_f16 v[34:37], v[114:115], v[170:171], v[34:37]
	v_mfma_f32_16x16x16_f16 v[50:53], v[116:117], v[174:175], v[50:53]
	v_mfma_f32_16x16x16_f16 v[34:37], v[116:117], v[178:179], v[34:37]
	v_mfma_f32_16x16x16_f16 v[110:113], v[198:199], v[108:109], v[50:53]
	v_mfma_f32_16x16x16_f16 v[58:61], v[198:199], v[56:57], v[34:37]
	v_mfma_f32_16x16x16_f16 v[34:37], v[48:49], v[134:135], 0
	v_mfma_f32_16x16x16_f16 v[50:53], v[46:47], v[136:137], 0
	v_mfma_f32_16x16x16_f16 v[102:105], v[118:119], v[136:137], 0
	v_mfma_f32_16x16x16_f16 v[138:141], v[126:127], v[160:161], 0
	s_nop 5
	v_sub_f32_e32 v37, v37, v53
	v_sub_f32_e32 v36, v36, v52
	v_sub_f32_e32 v35, v35, v51
	v_sub_f32_e32 v34, v34, v50
	v_mfma_f32_16x16x16_f16 v[50:53], v[196:197], v[164:165], v[94:97]
	v_mfma_f32_16x16x16_f16 v[50:53], v[202:203], v[174:175], v[50:53]
	v_mfma_f32_16x16x16_f16 v[94:97], v[210:211], v[108:109], v[50:53]
	v_mfma_f32_16x16x16_f16 v[50:53], v[120:121], v[134:135], 0
	v_mfma_f32_16x16x16_f16 v[34:37], v[100:101], v[162:163], v[34:37]
	v_mfma_f32_16x16x16_f16 v[166:169], v[122:123], v[160:161], 0
	s_nop 5
	v_sub_f32_e32 v53, v53, v105
	v_sub_f32_e32 v52, v52, v104
	v_sub_f32_e32 v51, v51, v103
	v_sub_f32_e32 v50, v50, v102
	v_mfma_f32_16x16x16_f16 v[102:105], v[206:207], v[164:165], v[138:141]
	v_mfma_f32_16x16x16_f16 v[138:141], v[72:73], v[134:135], 0
	v_mfma_f32_16x16x16_f16 v[134:137], v[70:71], v[136:137], 0
	v_mfma_f32_16x16x16_f16 v[50:53], v[126:127], v[162:163], v[50:53]
	v_mfma_f32_16x16x16_f16 v[34:37], v[196:197], v[170:171], v[34:37]
	s_nop 5
	v_sub_f32_e32 v137, v141, v137
	v_sub_f32_e32 v136, v140, v136
	v_sub_f32_e32 v135, v139, v135
	v_sub_f32_e32 v134, v138, v134
	v_mfma_f32_16x16x16_f16 v[50:53], v[206:207], v[170:171], v[50:53]
	s_nop 0
	v_mfma_f32_16x16x16_f16 v[134:137], v[122:123], v[162:163], v[134:137]
	ds_read_b128 v[160:163], v144 offset:6144
	v_mfma_f32_16x16x16_f16 v[134:137], v[200:201], v[170:171], v[134:137]
	v_mfma_f32_16x16x16_f16 v[138:141], v[200:201], v[164:165], v[166:169]
	v_mfma_f32_16x16x16_f16 v[34:37], v[202:203], v[178:179], v[34:37]
	v_mfma_f32_16x16x16_f16 v[50:53], v[204:205], v[178:179], v[50:53]
	v_mfma_f32_16x16x16_f16 v[134:137], v[146:147], v[178:179], v[134:137]
	v_mfma_f32_16x16x16_f16 v[102:105], v[204:205], v[174:175], v[102:105]
	v_mfma_f32_16x16x16_f16 v[138:141], v[146:147], v[174:175], v[138:141]
	v_mfma_f32_16x16x16_f16 v[34:37], v[210:211], v[56:57], v[34:37]
	v_mfma_f32_16x16x16_f16 v[50:53], v[208:209], v[56:57], v[50:53]
	v_mfma_f32_16x16x16_f16 v[54:57], v[142:143], v[56:57], v[134:137]
	v_mfma_f32_16x16x16_f16 v[134:137], v[64:65], v[130:131], 0
	v_mfma_f32_16x16x16_f16 v[62:65], v[62:63], v[132:133], 0
	v_mfma_f32_16x16x16_f16 v[102:105], v[208:209], v[108:109], v[102:105]
	v_mfma_f32_16x16x16_f16 v[106:109], v[142:143], v[108:109], v[138:141]
	s_nop 5
	v_sub_f32_e32 v65, v137, v65
	v_sub_f32_e32 v64, v136, v64
	v_sub_f32_e32 v63, v135, v63
	v_mfma_f32_16x16x16_f16 v[138:141], v[98:99], v[156:157], 0
	v_sub_f32_e32 v62, v134, v62
	s_nop 1
	v_mfma_f32_16x16x16_f16 v[62:65], v[98:99], v[148:149], v[62:65]
	v_mfma_f32_16x16x16_f16 v[134:137], v[114:115], v[154:155], v[138:141]
	v_mfma_f32_16x16x16_f16 v[62:65], v[114:115], v[152:153], v[62:65]
	v_mfma_f32_16x16x16_f16 v[134:137], v[116:117], v[158:159], v[134:137]
	v_mfma_f32_16x16x16_f16 v[62:65], v[116:117], v[150:151], v[62:65]
	v_mfma_f32_16x16x16_f16 v[114:117], v[198:199], v[124:125], v[134:137]
	v_mfma_f32_16x16x16_f16 v[134:137], v[48:49], v[130:131], 0
	v_mfma_f32_16x16x16_f16 v[46:49], v[46:47], v[132:133], 0
	v_mfma_f32_16x16x16_f16 v[138:141], v[100:101], v[156:157], 0
	v_mfma_f32_16x16x16_f16 v[62:65], v[198:199], v[128:129], v[62:65]
	s_nop 5
	v_sub_f32_e32 v49, v137, v49
	v_sub_f32_e32 v48, v136, v48
	v_sub_f32_e32 v47, v135, v47
	v_sub_f32_e32 v46, v134, v46
	v_mfma_f32_16x16x16_f16 v[134:137], v[120:121], v[130:131], 0
	v_mfma_f32_16x16x16_f16 v[118:121], v[118:119], v[132:133], 0
	v_mfma_f32_16x16x16_f16 v[46:49], v[100:101], v[148:149], v[46:49]
	v_mfma_f32_16x16x16_f16 v[98:101], v[196:197], v[154:155], v[138:141]
	s_nop 5
	v_sub_f32_e32 v121, v137, v121
	v_sub_f32_e32 v120, v136, v120
	v_sub_f32_e32 v119, v135, v119
	v_mfma_f32_16x16x16_f16 v[138:141], v[126:127], v[156:157], 0
	v_sub_f32_e32 v118, v134, v118
	s_nop 1
	v_mfma_f32_16x16x16_f16 v[118:121], v[126:127], v[148:149], v[118:121]
	v_ashrrev_i32_e32 v126, 3, v212
	v_ashrrev_i32_e32 v127, 31, v126
	v_lshl_add_u64 v[126:127], s[28:29], 0, v[126:127]
	v_mfma_f32_16x16x16_f16 v[134:137], v[206:207], v[154:155], v[138:141]
	v_lshlrev_b64 v[126:127], 11, v[126:127]
	v_mfma_f32_16x16x16_f16 v[118:121], v[206:207], v[152:153], v[118:121]
	v_mfma_f32_16x16x16_f16 v[138:141], v[72:73], v[130:131], 0
	v_mfma_f32_16x16x16_f16 v[70:73], v[70:71], v[132:133], 0
	v_mfma_f32_16x16x16_f16 v[134:137], v[204:205], v[158:159], v[134:137]
	v_mfma_f32_16x16x16_f16 v[46:49], v[196:197], v[152:153], v[46:49]
	s_nop 5
	v_sub_f32_e32 v133, v141, v73
	v_sub_f32_e32 v132, v140, v72
	v_sub_f32_e32 v131, v139, v71
	v_sub_f32_e32 v130, v138, v70
	v_mfma_f32_16x16x16_f16 v[70:73], v[204:205], v[150:151], v[118:121]
	v_and_or_b32 v138, v214, 56, s6
	v_lshlrev_b32_e32 v164, 1, v138
	v_or_b32_e32 v126, v126, v164
	v_mfma_f32_16x16x16_f16 v[118:121], v[208:209], v[124:125], v[134:137]
	s_nop 2
	ds_read_b128 v[134:137], v144
	v_mfma_f32_16x16x16_f16 v[138:141], v[122:123], v[156:157], 0
	v_lshl_add_u64 v[156:157], s[10:11], 0, v[126:127]
	s_waitcnt lgkmcnt(0)
	global_store_dwordx4 v[156:157], v[134:137], off
	v_mfma_f32_16x16x16_f16 v[130:133], v[122:123], v[148:149], v[130:133]
	v_lshl_add_u64 v[122:123], s[12:13], 0, v[126:127]
	v_add_u32_e32 v126, 64, v212
	global_store_dwordx4 v[122:123], v[160:163], off
	v_mfma_f32_16x16x16_f16 v[134:137], v[200:201], v[154:155], v[138:141]
	v_ashrrev_i32_e32 v122, 3, v126
	v_lshl_add_u32 v126, v126, 4, s36
	v_ashrrev_i32_e32 v123, 31, v122
	v_mfma_f32_16x16x16_f16 v[130:133], v[200:201], v[152:153], v[130:133]
	ds_read_b128 v[138:141], v126
	ds_read_b128 v[152:155], v126 offset:6144
	v_lshl_add_u64 v[122:123], s[28:29], 0, v[122:123]
	v_mfma_f32_16x16x16_f16 v[98:101], v[202:203], v[158:159], v[98:101]
	v_lshlrev_b64 v[122:123], 11, v[122:123]
	v_or_b32_e32 v122, v122, v164
	v_lshl_add_u64 v[126:127], s[10:11], 0, v[122:123]
	v_mfma_f32_16x16x16_f16 v[46:49], v[202:203], v[150:151], v[46:49]
	v_lshl_add_u64 v[122:123], s[12:13], 0, v[122:123]
	s_waitcnt lgkmcnt(1)
	global_store_dwordx4 v[126:127], v[138:141], off
	s_waitcnt lgkmcnt(0)
	global_store_dwordx4 v[122:123], v[152:155], off
	v_mfma_f32_16x16x16_f16 v[134:137], v[146:147], v[158:159], v[134:137]
	s_waitcnt lgkmcnt(0)
	v_mfma_f32_16x16x16_f16 v[130:133], v[146:147], v[150:151], v[130:133]
	v_mfma_f32_16x16x16_f16 v[98:101], v[210:211], v[124:125], v[98:101]
	v_mfma_f32_16x16x16_f16 v[46:49], v[210:211], v[128:129], v[46:49]
	v_mfma_f32_16x16x16_f16 v[70:73], v[208:209], v[128:129], v[70:73]
	v_mfma_f32_16x16x16_f16 v[122:125], v[142:143], v[124:125], v[134:137]
	v_mfma_f32_16x16x16_f16 v[126:129], v[142:143], v[128:129], v[130:133]
	s_cbranch_scc1 .LBB0_1287
.LBB0_1290:
	v_mov_b32_e32 v212, v1
	s_add_u32 s28, s41, s26
	s_addc_u32 s29, s42, s27
	v_and_b32_e32 v144, 15, v212
	v_and_b32_e32 v148, -16, v212
	v_lshl_add_u64 v[130:131], s[28:29], 0, v[144:145]
	v_ashrrev_i32_e32 v149, 31, v148
	v_lshlrev_b64 v[130:131], 10, v[130:131]
	v_lshl_add_u64 v[132:133], v[148:149], 0, s[6:7]
	v_lshl_add_u64 v[130:131], v[132:133], 0, v[130:131]
	v_lshlrev_b64 v[142:143], 1, v[130:131]
	v_lshl_add_u64 v[146:147], s[8:9], 0, v[142:143]
	global_load_dwordx4 v[130:133], v[146:147], off
	v_lshl_add_u64 v[138:139], s[14:15], 0, v[142:143]
	global_load_dwordx4 v[134:137], v[138:139], off
	s_nop 0
	global_load_dwordx4 v[138:141], v[138:139], off offset:16
	v_ashrrev_i32_e32 v179, 4, v212
	v_lshlrev_b32_e32 v178, 9, v179
	v_lshlrev_b32_e32 v180, 5, v144
	v_add3_u32 v149, s36, v178, v180
	v_mov_b32_e32 v161, 0
	v_cmp_eq_u32_e32 vcc, 15, v144
	s_mov_b64 s[96:97], vcc
	v_lshl_add_u32 v181, v148, 2, s36
	v_lshl_add_u32 v253, v148, 2, s36
	s_waitcnt vmcnt(1)
	ds_write_b128 v149, v[134:137] offset:12288
	s_waitcnt vmcnt(0)
	ds_write_b128 v149, v[138:141] offset:12304
	v_cvt_f32_f16_e32 v155, v130
	s_nop 1
	v_add_f32_dpp v134, v155, v155 row_shr:1 row_mask:0xf bank_mask:0xf bound_ctrl:1
	s_nop 0
	s_nop 0
	v_add_f32_dpp v134, v134, v134 row_shr:2 row_mask:0xf bank_mask:0xf bound_ctrl:1
	s_nop 0
	s_nop 0
	v_add_f32_dpp v172, v134, v134 row_shr:4 row_mask:0xf bank_mask:0xf bound_ctrl:1
	s_nop 0
	s_nop 0
	v_mov_b32_dpp v161, v172 row_shr:8 row_mask:0xf bank_mask:0xf
	s_nop 0


	v_cvt_f32_f16_sdwa v130, v130 dst_sel:DWORD dst_unused:UNUSED_PAD src0_sel:WORD_1
	v_mov_b32_e32 v148, 0
	s_nop 0
	v_add_f32_dpp v134, v130, v130 row_shr:1 row_mask:0xf bank_mask:0xf bound_ctrl:1
	s_nop 0
	s_nop 0
	v_add_f32_dpp v134, v134, v134 row_shr:2 row_mask:0xf bank_mask:0xf bound_ctrl:1
	s_nop 1
	v_add_f32_dpp v173, v134, v134 row_shr:4 row_mask:0xf bank_mask:0xf bound_ctrl:1
	s_nop 0
	s_nop 0
	v_mov_b32_dpp v148, v173 row_shr:8 row_mask:0xf bank_mask:0xf
	s_nop 0
	s_nop 1
	s_nop 0


	v_cvt_f32_f16_e32 v174, v131
	v_mov_b32_e32 v168, 0
	s_nop 0
	v_add_f32_dpp v134, v174, v174 row_shr:1 row_mask:0xf bank_mask:0xf bound_ctrl:1
	s_nop 0
	s_nop 0
	v_add_f32_dpp v134, v134, v134 row_shr:2 row_mask:0xf bank_mask:0xf bound_ctrl:1
	s_nop 1
	v_add_f32_dpp v177, v134, v134 row_shr:4 row_mask:0xf bank_mask:0xf bound_ctrl:1
	s_nop 0
	s_nop 0
	v_mov_b32_dpp v168, v177 row_shr:8 row_mask:0xf bank_mask:0xf
	s_nop 0
	s_nop 1
	s_nop 0


	v_cvt_f32_f16_sdwa v131, v131 dst_sel:DWORD dst_unused:UNUSED_PAD src0_sel:WORD_1
	v_mov_b32_e32 v166, 0
	s_nop 0
	v_add_f32_dpp v134, v131, v131 row_shr:1 row_mask:0xf bank_mask:0xf bound_ctrl:1
	s_nop 0
	s_nop 0
	v_add_f32_dpp v134, v134, v134 row_shr:2 row_mask:0xf bank_mask:0xf bound_ctrl:1
	s_nop 1
	v_add_f32_dpp v169, v134, v134 row_shr:4 row_mask:0xf bank_mask:0xf bound_ctrl:1
	s_nop 0
	s_nop 0
	v_mov_b32_dpp v166, v169 row_shr:8 row_mask:0xf bank_mask:0xf
	s_nop 0
	s_nop 1
	s_nop 0


	v_cvt_f32_f16_e32 v138, v132
	v_mov_b32_e32 v139, 0
	s_nop 0
	v_add_f32_dpp v134, v138, v138 row_shr:1 row_mask:0xf bank_mask:0xf bound_ctrl:1
	s_nop 0
	s_nop 0
	v_add_f32_dpp v134, v134, v134 row_shr:2 row_mask:0xf bank_mask:0xf bound_ctrl:1
	s_nop 1
	v_add_f32_dpp v141, v134, v134 row_shr:4 row_mask:0xf bank_mask:0xf bound_ctrl:1
	s_nop 0
	s_nop 0
	v_mov_b32_dpp v139, v141 row_shr:8 row_mask:0xf bank_mask:0xf
	s_nop 0
	s_nop 1
	s_nop 0


	v_cvt_f32_f16_sdwa v150, v132 dst_sel:DWORD dst_unused:UNUSED_PAD src0_sel:WORD_1
	v_mov_b32_e32 v134, 0
	s_nop 0
	v_add_f32_dpp v132, v150, v150 row_shr:1 row_mask:0xf bank_mask:0xf bound_ctrl:1
	s_nop 0
	s_nop 0
	v_add_f32_dpp v132, v132, v132 row_shr:2 row_mask:0xf bank_mask:0xf bound_ctrl:1
	s_nop 1
	v_add_f32_dpp v135, v132, v132 row_shr:4 row_mask:0xf bank_mask:0xf bound_ctrl:1
	s_nop 0
	s_nop 0
	v_mov_b32_dpp v134, v135 row_shr:8 row_mask:0xf bank_mask:0xf
	s_nop 0
	s_nop 1
	s_nop 0


	v_cvt_f32_f16_e32 v136, v133
	v_mov_b32_e32 v137, 0
	s_nop 0
	v_add_f32_dpp v132, v136, v136 row_shr:1 row_mask:0xf bank_mask:0xf bound_ctrl:1
	s_nop 0
	s_nop 0
	v_add_f32_dpp v132, v132, v132 row_shr:2 row_mask:0xf bank_mask:0xf bound_ctrl:1
	s_nop 1
	v_add_f32_dpp v153, v132, v132 row_shr:4 row_mask:0xf bank_mask:0xf bound_ctrl:1
	s_nop 0
	s_nop 0
	v_mov_b32_dpp v137, v153 row_shr:8 row_mask:0xf bank_mask:0xf
	s_nop 0
	s_nop 1
	s_nop 0


	v_cvt_f32_f16_sdwa v132, v133 dst_sel:DWORD dst_unused:UNUSED_PAD src0_sel:WORD_1
	v_mov_b32_e32 v156, 0
	s_nop 0
	v_add_f32_dpp v133, v132, v132 row_shr:1 row_mask:0xf bank_mask:0xf bound_ctrl:1
	s_nop 0
	s_nop 0
	v_add_f32_dpp v133, v133, v133 row_shr:2 row_mask:0xf bank_mask:0xf bound_ctrl:1
	s_nop 1
	v_add_f32_dpp v157, v133, v133 row_shr:4 row_mask:0xf bank_mask:0xf bound_ctrl:1
	s_nop 0
	s_nop 0
	v_mov_b32_dpp v156, v157 row_shr:8 row_mask:0xf bank_mask:0xf
	s_nop 0
	s_nop 1
	s_nop 0


	v_add_f32_e32 v137, v153, v137
	s_nop 1
	v_mov_b32_dpp v152, v137 row_newbcast:15 row_mask:0xf bank_mask:0xf
	v_sub_f32_e32 v136, v137, v136
	v_mul_f32_e32 v153, 0x3fb8aa3b, v137
	v_mul_f32_e32 v136, 0x3fb8aa3b, v136
	v_exp_f32_e32 v154, v153
	s_mov_b64 exec, s[96:97]
	ds_write_b32 v253, v154 offset:16408
	s_mov_b64 exec, -1
	v_mul_f32_e32 v153, 0xbfb8aa3b, v137
	v_exp_f32_e32 v162, v136
	v_sub_f32_e32 v136, v152, v137
	v_add_f32_e32 v188, v157, v156
	s_nop 1
	v_mov_b32_dpp v133, v188 row_newbcast:15 row_mask:0xf bank_mask:0xf
	v_add_f32_e32 v156, v135, v134
	s_nop 1
	v_mov_b32_dpp v151, v156 row_newbcast:15 row_mask:0xf bank_mask:0xf
	v_exp_f32_e32 v159, v153
	v_mul_f32_e32 v136, 0x3fb8aa3b, v136
	v_mul_f32_e32 v134, 0x3fb8aa3b, v156
	v_lshl_add_u64 v[152:153], s[16:17], 0, v[142:143]
	v_exp_f32_e32 v160, v136
	v_exp_f32_e32 v157, v134
	s_mov_b64 exec, s[96:97]
	ds_write_b32 v253, v157 offset:16404
	s_mov_b64 exec, -1
	global_load_dwordx4 v[134:137], v[152:153], off
	v_sub_f32_e32 v150, v156, v150
	v_mul_f32_e32 v150, 0x3fb8aa3b, v150
	v_add_f32_e32 v139, v141, v139
	s_nop 1
	v_mov_b32_dpp v140, v139 row_newbcast:15 row_mask:0xf bank_mask:0xf
	v_exp_f32_e32 v171, v150
	v_sub_f32_e32 v150, v151, v156
	v_sub_f32_e32 v138, v139, v138
	v_mul_f32_e32 v150, 0x3fb8aa3b, v150
	v_mul_f32_e32 v141, 0x3fb8aa3b, v139
	v_mul_f32_e32 v138, 0x3fb8aa3b, v138
	v_mul_f32_e32 v158, 0xbfb8aa3b, v156
	v_exp_f32_e32 v165, v150
	v_exp_f32_e32 v156, v141
	s_mov_b64 exec, s[96:97]
	ds_write_b32 v253, v156 offset:16400
	s_mov_b64 exec, -1
	v_mul_f32_e32 v141, 0xbfb8aa3b, v139
	v_exp_f32_e32 v170, v138
	v_sub_f32_e32 v138, v140, v139
	v_lshl_add_u64 v[150:151], s[18:19], 0, v[142:143]
	v_exp_f32_e32 v167, v141
	v_mul_f32_e32 v164, 0x3fb8aa3b, v138
	global_load_dwordx4 v[138:141], v[150:151], off
	v_add_f32_e32 v182, v169, v166
	s_nop 1
	v_mov_b32_dpp v175, v182 row_newbcast:15 row_mask:0xf bank_mask:0xf
	v_sub_f32_e32 v131, v182, v131
	v_mul_f32_e32 v131, 0x3fb8aa3b, v131
	v_exp_f32_e32 v191, v131
	v_sub_f32_e32 v131, v175, v182
	v_mul_f32_e32 v131, 0x3fb8aa3b, v131
	v_exp_f32_e32 v175, v131
	v_add_f32_e32 v131, v177, v168
	s_nop 1
	v_mov_b32_dpp v176, v131 row_newbcast:15 row_mask:0xf bank_mask:0xf
	v_mul_f32_e32 v168, 0x3fb8aa3b, v131
	v_mul_f32_e32 v177, 0xbfb8aa3b, v131
	v_sub_f32_e32 v174, v131, v174
	v_sub_f32_e32 v131, v176, v131
	v_mul_f32_e32 v174, 0x3fb8aa3b, v174
	v_mul_f32_e32 v131, 0x3fb8aa3b, v131
	v_exp_f32_e32 v190, v174
	v_exp_f32_e32 v174, v131
	v_add_f32_e32 v131, v173, v148
	s_nop 1
	v_mov_b32_dpp v149, v131 row_newbcast:15 row_mask:0xf bank_mask:0xf
	v_mul_f32_e32 v148, 0x3fb8aa3b, v131
	v_sub_f32_e32 v130, v131, v130
	v_exp_f32_e32 v173, v148
	s_mov_b64 exec, s[96:97]
	ds_write_b32 v253, v173 offset:16388
	s_mov_b64 exec, -1
	v_mul_f32_e32 v148, 0xbfb8aa3b, v131
	v_mul_f32_e32 v130, 0x3fb8aa3b, v130
	v_mul_f32_e32 v166, 0x3fb8aa3b, v182
	v_exp_f32_e32 v176, v148
	v_exp_f32_e32 v187, v130
	v_sub_f32_e32 v130, v149, v131
	v_lshl_add_u64 v[148:149], s[20:21], 0, v[142:143]
	v_exp_f32_e32 v169, v166
	s_mov_b64 exec, s[96:97]
	ds_write_b32 v253, v169 offset:16396
	s_mov_b64 exec, -1
	v_mul_f32_e32 v166, 0xbfb8aa3b, v182
	global_load_dwordx4 v[182:185], v[148:149], off
	v_mul_f32_e32 v130, 0x3fb8aa3b, v130
	v_exp_f32_e32 v195, v130
	v_add_f32_e32 v130, v172, v161
	s_nop 1
	v_mov_b32_dpp v163, v130 row_newbcast:15 row_mask:0xf bank_mask:0xf
	v_mul_f32_e32 v131, 0x3fb8aa3b, v130
	v_exp_f32_e32 v172, v131
	s_mov_b64 exec, s[96:97]
	ds_write_b32 v253, v172 offset:16384
	s_mov_b64 exec, -1
	v_mul_f32_e32 v131, 0xbfb8aa3b, v130
	v_exp_f32_e32 v196, v131
	v_sub_f32_e32 v131, v130, v155
	v_sub_f32_e32 v130, v163, v130
	v_mul_f32_e32 v130, 0x3fb8aa3b, v130
	v_exp_f32_e32 v194, v130
	v_mul_f32_e32 v130, 0x3fb8aa3b, v188
	v_exp_f32_e32 v155, v130
	s_mov_b64 exec, s[96:97]
	ds_write_b32 v253, v155 offset:16412
	s_mov_b64 exec, -1
	v_mul_f32_e32 v130, 0xbfb8aa3b, v188
	v_exp_f32_e32 v198, v130
	v_sub_f32_e32 v130, v188, v132
	v_mul_f32_e32 v130, 0x3fb8aa3b, v130
	v_mul_f32_e32 v131, 0x3fb8aa3b, v131
	v_exp_f32_e32 v163, v130
	v_sub_f32_e32 v130, v133, v188
	v_exp_f32_e32 v186, v131
	v_mul_f32_e32 v161, 0x3fb8aa3b, v130
	global_load_dwordx4 v[130:133], v[146:147], off offset:16
	v_lshl_add_u64 v[142:143], s[22:23], 0, v[142:143]
	v_or_b32_e32 v197, v180, v178
	v_exp_f32_e32 v177, v177
	v_exp_f32_e32 v166, v166
	v_exp_f32_e32 v164, v164
	v_exp_f32_e32 v158, v158
	v_exp_f32_e32 v161, v161
	s_waitcnt vmcnt(3)
	v_cvt_f32_f16_e32 v146, v134
	v_cvt_f32_f16_sdwa v147, v134 dst_sel:DWORD dst_unused:UNUSED_PAD src0_sel:WORD_1
	v_cvt_f32_f16_e32 v192, v135
	v_cvt_f32_f16_sdwa v193, v135 dst_sel:DWORD dst_unused:UNUSED_PAD src0_sel:WORD_1
	v_exp_f32_e32 v168, v168
	s_mov_b64 exec, s[96:97]
	ds_write_b32 v253, v168 offset:16392
	s_mov_b64 exec, -1
	v_mul_f32_e32 v134, v186, v146
	v_mul_f32_e32 v135, v187, v147
	global_load_dwordx4 v[186:189], v[142:143], off
	v_mul_f32_e32 v146, v190, v192
	v_mul_f32_e32 v147, v191, v193
	v_cvt_f32_f16_e32 v190, v136
	v_cvt_f32_f16_sdwa v191, v136 dst_sel:DWORD dst_unused:UNUSED_PAD src0_sel:WORD_1
	v_cvt_f32_f16_e32 v192, v137
	v_cvt_f32_f16_sdwa v193, v137 dst_sel:DWORD dst_unused:UNUSED_PAD src0_sel:WORD_1
	v_cvt_pk_f16_f32 v134, v134, v135
	v_cvt_pk_f16_f32 v135, v146, v147
	v_mul_f32_e32 v136, v170, v190
	v_mul_f32_e32 v137, v171, v191
	v_mul_f32_e32 v146, v162, v192
	v_mul_f32_e32 v147, v163, v193
	v_cvt_pk_f16_f32 v136, v136, v137
	v_cvt_pk_f16_f32 v137, v146, v147
	v_add_u32_e32 v147, s36, v197
	ds_write_b128 v147, v[134:137]
	s_waitcnt vmcnt(3)
	v_cvt_f32_f16_e32 v136, v138
	v_cvt_f32_f16_sdwa v137, v138 dst_sel:DWORD dst_unused:UNUSED_PAD src0_sel:WORD_1
	v_cvt_f32_f16_e32 v162, v139
	v_cvt_f32_f16_sdwa v163, v139 dst_sel:DWORD dst_unused:UNUSED_PAD src0_sel:WORD_1
	v_fma_mixlo_f16 v146, v196, v138, 0 op_sel_hi:[0,1,0]
	v_cvt_f32_f16_e32 v138, v140
	v_cvt_f32_f16_sdwa v139, v140 dst_sel:DWORD dst_unused:UNUSED_PAD src0_sel:WORD_1
	v_mul_f32_e32 v134, v194, v136
	v_mul_f32_e32 v135, v195, v137
	v_mov_b32_e32 v136, v137
	v_mov_b32_e32 v137, v162
	v_cvt_pk_f16_f32 v134, v134, v135
	v_mul_f32_e32 v136, v176, v136
	v_mul_f32_e32 v137, v177, v137
	s_nop 0
	v_cvt_pk_f16_f32 v170, v136, v137
	v_mul_f32_e32 v136, v174, v162
	v_mul_f32_e32 v137, v175, v163
	v_pack_b32_f16 v190, v146, v170
	v_cvt_pk_f16_f32 v135, v136, v137
	v_mov_b32_e32 v136, v163
	v_mov_b32_e32 v137, v138
	v_cvt_f32_f16_e32 v162, v141
	v_cvt_f32_f16_sdwa v163, v141 dst_sel:DWORD dst_unused:UNUSED_PAD src0_sel:WORD_1
	v_mul_f32_e32 v136, v166, v136
	v_mul_f32_e32 v137, v167, v137
	s_nop 0
	v_cvt_pk_f16_f32 v140, v136, v137
	v_mul_f32_e32 v136, v164, v138
	v_mul_f32_e32 v137, v165, v139
	v_mov_b32_e32 v138, v139
	v_mov_b32_e32 v139, v162
	v_cvt_pk_f16_f32 v136, v136, v137
	v_mul_f32_e32 v138, v158, v138
	v_mul_f32_e32 v139, v159, v139
	v_alignbit_b32 v191, v140, v170, 16
	v_cvt_pk_f16_f32 v137, v138, v139
	v_lshrrev_b32_e32 v193, 16, v137
	v_mul_f32_e32 v138, v160, v162
	v_mul_f32_e32 v139, v161, v163
	v_alignbit_b32 v192, v137, v140, 16
	v_cvt_pk_f16_f32 v137, v138, v139
	v_fma_mixhi_f16 v193, v198, v141, 0 op_sel:[0,1,0] op_sel_hi:[0,1,0]
	ds_write_b128 v147, v[190:193] offset:2048
	ds_write_b128 v147, v[134:137] offset:8192
	s_waitcnt vmcnt(2)
	v_cvt_f32_f16_e32 v136, v182
	v_cvt_f32_f16_sdwa v137, v182 dst_sel:DWORD dst_unused:UNUSED_PAD src0_sel:WORD_1
	v_cvt_f32_f16_e32 v140, v183
	v_cvt_f32_f16_sdwa v141, v183 dst_sel:DWORD dst_unused:UNUSED_PAD src0_sel:WORD_1
	v_cvt_f32_f16_e32 v162, v184
	v_cvt_f32_f16_sdwa v163, v184 dst_sel:DWORD dst_unused:UNUSED_PAD src0_sel:WORD_1
	v_mul_f32_e32 v134, v194, v136
	v_mul_f32_e32 v135, v195, v137
	v_mov_b32_e32 v136, v137
	v_mov_b32_e32 v137, v140
	v_cvt_pk_f16_f32 v134, v134, v135
	v_mul_f32_e32 v136, v176, v136
	v_mul_f32_e32 v137, v177, v137
	v_fma_mixlo_f16 v138, v196, v182, 0 op_sel_hi:[0,1,0]
	v_cvt_pk_f16_f32 v139, v136, v137
	v_mul_f32_e32 v136, v174, v140
	v_mul_f32_e32 v137, v175, v141
	v_pack_b32_f16 v138, v138, v139
	v_cvt_pk_f16_f32 v135, v136, v137
	v_mov_b32_e32 v136, v141
	v_mov_b32_e32 v137, v162
	s_nop 0
	v_mul_f32_e32 v136, v166, v136
	v_mul_f32_e32 v137, v167, v137
	v_cvt_f32_f16_e32 v166, v185
	v_cvt_f32_f16_sdwa v167, v185 dst_sel:DWORD dst_unused:UNUSED_PAD src0_sel:WORD_1
	v_cvt_pk_f16_f32 v146, v136, v137
	v_mul_f32_e32 v136, v164, v162
	v_mul_f32_e32 v137, v165, v163
	v_alignbit_b32 v139, v146, v139, 16
	v_mov_b32_e32 v140, v163
	v_mov_b32_e32 v141, v166
	v_cvt_pk_f16_f32 v136, v136, v137
	v_mul_f32_e32 v140, v158, v140
	v_mul_f32_e32 v141, v159, v141
	v_mul_f32_e32 v158, v160, v166
	v_mul_f32_e32 v159, v161, v167
	v_cvt_pk_f16_f32 v137, v140, v141
	v_lshrrev_b32_e32 v141, 16, v137
	v_alignbit_b32 v140, v137, v146, 16
	v_fma_mixhi_f16 v141, v198, v185, 0 op_sel:[0,1,0] op_sel_hi:[0,1,0]
	ds_write_b128 v147, v[138:141] offset:4096
	s_waitcnt vmcnt(0)
	v_cvt_f32_f16_e32 v138, v186
	v_cvt_f32_f16_sdwa v139, v186 dst_sel:DWORD dst_unused:UNUSED_PAD src0_sel:WORD_1
	v_cvt_pk_f16_f32 v137, v158, v159
	v_cvt_f32_f16_e32 v140, v187
	v_cvt_f32_f16_sdwa v141, v187 dst_sel:DWORD dst_unused:UNUSED_PAD src0_sel:WORD_1
	ds_write_b128 v147, v[134:137] offset:10240
	v_cvt_f32_f16_e32 v136, v188
	v_cvt_f32_f16_sdwa v137, v188 dst_sel:DWORD dst_unused:UNUSED_PAD src0_sel:WORD_1
	v_mul_f32_e32 v134, v172, v138
	v_mul_f32_e32 v135, v173, v139
	v_mul_f32_e32 v136, v156, v136
	v_mul_f32_e32 v137, v157, v137
	v_cvt_pk_f16_f32 v138, v134, v135
	v_mul_f32_e32 v134, v168, v140
	v_mul_f32_e32 v135, v169, v141
	v_cvt_pk_f16_f32 v140, v136, v137
	v_cvt_pk_f16_f32 v139, v134, v135
	v_cvt_f32_f16_e32 v134, v189
	v_cvt_f32_f16_sdwa v135, v189 dst_sel:DWORD dst_unused:UNUSED_PAD src0_sel:WORD_1
	v_cvt_f32_f16_e32 v137, v130
	v_mul_f32_e32 v134, v154, v134
	v_mul_f32_e32 v135, v155, v135
	s_nop 0
	v_cvt_pk_f16_f32 v141, v134, v135
	v_add_f32_dpp v134, v137, v137 row_shr:1 row_mask:0xf bank_mask:0xf bound_ctrl:1
	ds_write_b128 v147, v[138:141] offset:6144
	v_mov_b32_e32 v154, 0
	v_add_f32_dpp v134, v134, v134 row_shr:2 row_mask:0xf bank_mask:0xf bound_ctrl:1
	s_nop 1
	v_add_f32_dpp v139, v134, v134 row_shr:4 row_mask:0xf bank_mask:0xf bound_ctrl:1
	s_nop 0
	s_nop 0
	v_mov_b32_dpp v154, v139 row_shr:8 row_mask:0xf bank_mask:0xf
	s_nop 0
	s_nop 1
	s_nop 0
	s_nop 1
	s_nop 0


	v_cvt_f32_f16_sdwa v156, v130 dst_sel:DWORD dst_unused:UNUSED_PAD src0_sel:WORD_1
	v_mov_b32_e32 v158, 0
	s_nop 0
	v_add_f32_dpp v130, v156, v156 row_shr:1 row_mask:0xf bank_mask:0xf bound_ctrl:1
	s_nop 0
	s_nop 0
	v_add_f32_dpp v130, v130, v130 row_shr:2 row_mask:0xf bank_mask:0xf bound_ctrl:1
	s_nop 1
	v_add_f32_dpp v159, v130, v130 row_shr:4 row_mask:0xf bank_mask:0xf bound_ctrl:1
	s_nop 0
	s_nop 0
	v_mov_b32_dpp v158, v159 row_shr:8 row_mask:0xf bank_mask:0xf
	s_nop 0
	s_nop 1
	s_nop 0


	v_cvt_f32_f16_e32 v160, v131
	v_mov_b32_e32 v161, 0
	s_nop 0
	v_add_f32_dpp v130, v160, v160 row_shr:1 row_mask:0xf bank_mask:0xf bound_ctrl:1
	s_nop 0
	s_nop 0
	v_add_f32_dpp v130, v130, v130 row_shr:2 row_mask:0xf bank_mask:0xf bound_ctrl:1
	s_nop 1
	v_add_f32_dpp v163, v130, v130 row_shr:4 row_mask:0xf bank_mask:0xf bound_ctrl:1
	s_nop 0
	s_nop 0
	v_mov_b32_dpp v161, v163 row_shr:8 row_mask:0xf bank_mask:0xf
	s_nop 0
	s_nop 1
	s_nop 0


	v_cvt_f32_f16_sdwa v131, v131 dst_sel:DWORD dst_unused:UNUSED_PAD src0_sel:WORD_1
	v_mov_b32_e32 v165, 0
	s_nop 0
	v_add_f32_dpp v130, v131, v131 row_shr:1 row_mask:0xf bank_mask:0xf bound_ctrl:1
	s_nop 0
	s_nop 0
	v_add_f32_dpp v130, v130, v130 row_shr:2 row_mask:0xf bank_mask:0xf bound_ctrl:1
	s_nop 1
	v_add_f32_dpp v167, v130, v130 row_shr:4 row_mask:0xf bank_mask:0xf bound_ctrl:1
	s_nop 0
	s_nop 0
	v_mov_b32_dpp v165, v167 row_shr:8 row_mask:0xf bank_mask:0xf
	s_nop 0
	s_nop 1
	s_nop 0


	v_cvt_f32_f16_e32 v140, v132
	v_mov_b32_e32 v134, 0
	s_nop 0
	v_add_f32_dpp v130, v140, v140 row_shr:1 row_mask:0xf bank_mask:0xf bound_ctrl:1
	s_nop 0
	s_nop 0
	v_add_f32_dpp v130, v130, v130 row_shr:2 row_mask:0xf bank_mask:0xf bound_ctrl:1
	s_nop 1
	v_add_f32_dpp v170, v130, v130 row_shr:4 row_mask:0xf bank_mask:0xf bound_ctrl:1
	s_nop 0
	s_nop 0
	v_mov_b32_dpp v134, v170 row_shr:8 row_mask:0xf bank_mask:0xf
	s_nop 0
	s_nop 1
	s_nop 0


	v_cvt_f32_f16_sdwa v141, v132 dst_sel:DWORD dst_unused:UNUSED_PAD src0_sel:WORD_1
	v_mov_b32_e32 v132, 0
	s_nop 0
	v_add_f32_dpp v130, v141, v141 row_shr:1 row_mask:0xf bank_mask:0xf bound_ctrl:1
	s_nop 0
	s_nop 0
	v_add_f32_dpp v130, v130, v130 row_shr:2 row_mask:0xf bank_mask:0xf bound_ctrl:1
	s_nop 1
	v_add_f32_dpp v135, v130, v130 row_shr:4 row_mask:0xf bank_mask:0xf bound_ctrl:1
	s_nop 0
	s_nop 0
	v_mov_b32_dpp v132, v135 row_shr:8 row_mask:0xf bank_mask:0xf
	s_nop 0
	s_nop 1
	s_nop 0


	v_cvt_f32_f16_e32 v136, v133
	v_mov_b32_e32 v130, 0
	s_nop 0
	v_add_f32_dpp v138, v136, v136 row_shr:1 row_mask:0xf bank_mask:0xf bound_ctrl:1
	s_nop 0
	s_nop 0
	v_add_f32_dpp v138, v138, v138 row_shr:2 row_mask:0xf bank_mask:0xf bound_ctrl:1
	s_nop 1
	v_add_f32_dpp v174, v138, v138 row_shr:4 row_mask:0xf bank_mask:0xf bound_ctrl:1
	s_nop 0
	s_nop 0
	v_mov_b32_dpp v130, v174 row_shr:8 row_mask:0xf bank_mask:0xf
	s_nop 0
	s_nop 1
	s_nop 0


	v_cvt_f32_f16_sdwa v164, v133 dst_sel:DWORD dst_unused:UNUSED_PAD src0_sel:WORD_1
	v_mov_b32_e32 v172, 0
	s_nop 0
	v_add_f32_dpp v133, v164, v164 row_shr:1 row_mask:0xf bank_mask:0xf bound_ctrl:1
	s_nop 0
	s_nop 0
	v_add_f32_dpp v133, v133, v133 row_shr:2 row_mask:0xf bank_mask:0xf bound_ctrl:1
	s_nop 1
	v_add_f32_dpp v173, v133, v133 row_shr:4 row_mask:0xf bank_mask:0xf bound_ctrl:1
	s_nop 0
	v_mov_b32_e32 v146, 0
	v_mov_b32_dpp v172, v173 row_shr:8 row_mask:0xf bank_mask:0xf
	s_nop 0
	s_nop 1
	s_nop 0


	v_cndmask_b32_e64 v146, 0, 1.0, s[96:97]
	v_add_f32_e32 v174, v174, v130
	s_nop 1
	v_mov_b32_dpp v138, v174 row_newbcast:15 row_mask:0xf bank_mask:0xf
	v_mul_f32_e32 v130, 0x3fb8aa3b, v174
	v_mul_f32_e32 v133, 0xbfb8aa3b, v174
	v_sub_f32_e32 v136, v174, v136
	v_sub_f32_e32 v138, v138, v174
	global_load_dwordx4 v[174:177], v[152:153], off offset:16
	v_add_f32_e32 v152, v135, v132
	s_nop 1
	v_mov_b32_dpp v171, v152 row_newbcast:15 row_mask:0xf bank_mask:0xf
	v_sub_f32_e32 v141, v152, v141
	v_mul_f32_e32 v132, 0x3fb8aa3b, v152
	v_mul_f32_e32 v141, 0x3fb8aa3b, v141
	v_add_f32_e32 v181, v173, v172
	s_nop 1
	v_mov_b32_dpp v168, v181 row_newbcast:15 row_mask:0xf bank_mask:0xf
	v_exp_f32_e32 v135, v132
	s_mov_b64 exec, s[96:97]
	ds_write_b32 v253, v135 offset:16436
	s_mov_b64 exec, -1
	v_mul_f32_e32 v132, 0xbfb8aa3b, v152
	v_exp_f32_e32 v183, v141
	v_sub_f32_e32 v141, v171, v152
	v_add_f32_e32 v152, v170, v134
	s_nop 1
	v_mov_b32_dpp v169, v152 row_newbcast:15 row_mask:0xf bank_mask:0xf
	global_load_dwordx4 v[170:173], v[150:151], off offset:16
	v_add_f32_e32 v150, v167, v165
	s_nop 1
	v_mov_b32_dpp v166, v150 row_newbcast:15 row_mask:0xf bank_mask:0xf
	v_sub_f32_e32 v131, v150, v131
	v_mul_f32_e32 v131, 0x3fb8aa3b, v131
	v_exp_f32_e32 v167, v131
	v_sub_f32_e32 v131, v166, v150
	v_sub_f32_e32 v140, v152, v140
	v_mul_f32_e32 v131, 0x3fb8aa3b, v131
	v_mul_f32_e32 v140, 0x3fb8aa3b, v140
	v_exp_f32_e32 v185, v131
	v_add_f32_e32 v131, v163, v161
	s_nop 1
	v_mov_b32_dpp v162, v131 row_newbcast:15 row_mask:0xf bank_mask:0xf
	v_mul_f32_e32 v134, 0x3fb8aa3b, v152
	v_mul_f32_e32 v153, 0xbfb8aa3b, v152
	v_exp_f32_e32 v182, v140
	v_sub_f32_e32 v140, v169, v152
	v_mul_f32_e32 v151, 0x3fb8aa3b, v150
	v_mul_f32_e32 v152, 0xbfb8aa3b, v150
	v_mul_f32_e32 v150, 0x3fb8aa3b, v131
	v_mul_f32_e32 v161, 0xbfb8aa3b, v131
	v_sub_f32_e32 v160, v131, v160
	v_sub_f32_e32 v131, v162, v131
	v_mul_f32_e32 v131, 0x3fb8aa3b, v131
	v_exp_f32_e32 v184, v131
	v_add_f32_e32 v131, v159, v158
	s_nop 1
	v_mov_b32_dpp v157, v131 row_newbcast:15 row_mask:0xf bank_mask:0xf
	v_mul_f32_e32 v160, 0x3fb8aa3b, v160
	v_mul_f32_e32 v158, 0x3fb8aa3b, v131
	v_exp_f32_e32 v187, v161
	v_exp_f32_e32 v166, v160
	v_exp_f32_e32 v189, v158
	s_mov_b64 exec, s[96:97]
	ds_write_b32 v253, v189 offset:16420
	s_mov_b64 exec, -1
	global_load_dwordx4 v[158:161], v[148:149], off offset:16
	v_mul_f32_e32 v162, 0xbfb8aa3b, v131
	v_sub_f32_e32 v148, v131, v156
	v_sub_f32_e32 v131, v157, v131
	v_mul_f32_e32 v131, 0x3fb8aa3b, v131
	v_exp_f32_e32 v191, v131
	v_add_f32_e32 v131, v139, v154
	s_nop 1
	v_mov_b32_dpp v155, v131 row_newbcast:15 row_mask:0xf bank_mask:0xf
	v_mul_f32_e32 v139, 0x3fb8aa3b, v131
	v_exp_f32_e32 v188, v139
	s_mov_b64 exec, s[96:97]
	ds_write_b32 v253, v188 offset:16416
	s_mov_b64 exec, -1
	v_mul_f32_e32 v139, 0xbfb8aa3b, v131
	v_sub_f32_e32 v137, v131, v137
	v_sub_f32_e32 v131, v155, v131
	global_load_dwordx4 v[154:157], v[142:143], off offset:16
	v_mul_f32_e32 v148, 0x3fb8aa3b, v148
	v_mul_f32_e32 v137, 0x3fb8aa3b, v137
	v_exp_f32_e32 v186, v162
	v_exp_f32_e32 v149, v148
	v_exp_f32_e32 v148, v137
	v_mul_f32_e32 v137, 0xbfb8aa3b, v181
	v_exp_f32_e32 v193, v137
	v_sub_f32_e32 v137, v181, v164
	v_mul_f32_e32 v136, 0x3fb8aa3b, v136
	v_mul_f32_e32 v137, 0x3fb8aa3b, v137
	v_exp_f32_e32 v136, v136
	v_exp_f32_e32 v137, v137
	v_mul_f32_e32 v131, 0x3fb8aa3b, v131
	v_exp_f32_e32 v190, v131
	v_exp_f32_e32 v153, v153
	v_exp_f32_e32 v152, v152
	v_mul_f32_e32 v141, 0x3fb8aa3b, v141
	v_mul_f32_e32 v140, 0x3fb8aa3b, v140
	v_exp_f32_e32 v192, v139
	v_exp_f32_e32 v141, v141
	v_exp_f32_e32 v140, v140
	v_exp_f32_e32 v133, v133
	v_exp_f32_e32 v132, v132
	v_sub_f32_e32 v139, v168, v181
	v_mul_f32_e32 v138, 0x3fb8aa3b, v138
	v_mul_f32_e32 v139, 0x3fb8aa3b, v139
	v_exp_f32_e32 v138, v138
	s_waitcnt vmcnt(3)
	v_cvt_f32_f16_sdwa v163, v174 dst_sel:DWORD dst_unused:UNUSED_PAD src0_sel:WORD_1
	v_cvt_f32_f16_e32 v162, v174
	v_cvt_f32_f16_sdwa v165, v175 dst_sel:DWORD dst_unused:UNUSED_PAD src0_sel:WORD_1
	v_cvt_f32_f16_e32 v164, v175
	v_exp_f32_e32 v139, v139
	v_mul_f32_e32 v142, v148, v162
	v_mul_f32_e32 v143, v149, v163
	v_cvt_f32_f16_sdwa v149, v176 dst_sel:DWORD dst_unused:UNUSED_PAD src0_sel:WORD_1
	v_cvt_pk_f16_f32 v162, v142, v143
	v_mul_f32_e32 v142, v166, v164
	v_mul_f32_e32 v143, v167, v165
	v_cvt_f32_f16_e32 v148, v176
	v_cvt_f32_f16_sdwa v167, v177 dst_sel:DWORD dst_unused:UNUSED_PAD src0_sel:WORD_1
	v_cvt_f32_f16_e32 v166, v177
	v_cvt_pk_f16_f32 v163, v142, v143
	v_mul_f32_e32 v142, v182, v148
	v_mul_f32_e32 v143, v183, v149
	v_mul_f32_e32 v131, 0x3fb8aa3b, v181
	v_mul_f32_e32 v136, v136, v166
	v_mul_f32_e32 v137, v137, v167
	v_cvt_pk_f16_f32 v164, v142, v143
	v_cvt_pk_f16_f32 v165, v136, v137
	s_waitcnt vmcnt(2)
	v_cvt_f32_f16_sdwa v137, v170 dst_sel:DWORD dst_unused:UNUSED_PAD src0_sel:WORD_1
	v_cvt_f32_f16_e32 v136, v170
	v_cvt_f32_f16_sdwa v143, v171 dst_sel:DWORD dst_unused:UNUSED_PAD src0_sel:WORD_1
	v_cvt_f32_f16_e32 v142, v171
	ds_write_b128 v147, v[162:165] offset:16
	v_mul_f32_e32 v148, v190, v136
	v_mul_f32_e32 v149, v191, v137
	v_fma_mixlo_f16 v163, v192, v170, 0 op_sel_hi:[0,1,0]
	v_mov_b32_e32 v136, v137
	v_mov_b32_e32 v137, v142
	v_cvt_pk_f16_f32 v162, v148, v149
	v_mul_f32_e32 v136, v186, v136
	v_mul_f32_e32 v137, v187, v137
	v_mul_f32_e32 v148, v184, v142
	v_mul_f32_e32 v149, v185, v143
	v_cvt_pk_f16_f32 v164, v136, v137
	v_cvt_f32_f16_sdwa v137, v172 dst_sel:DWORD dst_unused:UNUSED_PAD src0_sel:WORD_1
	v_cvt_f32_f16_e32 v136, v172
	v_pack_b32_f16 v166, v163, v164
	v_cvt_pk_f16_f32 v163, v148, v149
	v_exp_f32_e32 v130, v130
	s_mov_b64 exec, s[96:97]
	ds_write_b32 v253, v130 offset:16440
	s_mov_b64 exec, -1
	v_mov_b32_e32 v142, v143
	v_mov_b32_e32 v143, v136
	v_mul_f32_e32 v148, v140, v136
	v_mul_f32_e32 v149, v141, v137
	v_mul_f32_e32 v142, v152, v142
	v_mul_f32_e32 v143, v153, v143
	v_exp_f32_e32 v134, v134
	s_mov_b64 exec, s[96:97]
	ds_write_b32 v253, v134 offset:16432
	s_mov_b64 exec, -1
	v_cvt_pk_f16_f32 v165, v142, v143
	v_cvt_f32_f16_sdwa v143, v173 dst_sel:DWORD dst_unused:UNUSED_PAD src0_sel:WORD_1
	v_cvt_f32_f16_e32 v142, v173
	v_alignbit_b32 v167, v165, v164, 16
	v_cvt_pk_f16_f32 v164, v148, v149
	v_exp_f32_e32 v151, v151
	s_mov_b64 exec, s[96:97]
	ds_write_b32 v253, v151 offset:16428
	s_mov_b64 exec, -1
	v_mov_b32_e32 v136, v137
	v_mov_b32_e32 v137, v142
	v_exp_f32_e32 v150, v150
	s_mov_b64 exec, s[96:97]
	ds_write_b32 v253, v150 offset:16424
	s_mov_b64 exec, -1
	v_mul_f32_e32 v136, v132, v136
	v_mul_f32_e32 v137, v133, v137
	v_exp_f32_e32 v131, v131
	s_mov_b64 exec, s[96:97]
	ds_write_b32 v253, v131 offset:16444
	s_mov_b64 exec, -1
	v_cvt_pk_f16_f32 v136, v136, v137
	v_alignbit_b32 v168, v136, v165, 16
	v_lshrrev_b32_e32 v169, 16, v136
	v_mul_f32_e32 v136, v138, v142
	v_mul_f32_e32 v137, v139, v143
	s_waitcnt vmcnt(1)
	v_cvt_f32_f16_sdwa v143, v159 dst_sel:DWORD dst_unused:UNUSED_PAD src0_sel:WORD_1
	v_cvt_pk_f16_f32 v165, v136, v137
	v_cvt_f32_f16_sdwa v137, v158 dst_sel:DWORD dst_unused:UNUSED_PAD src0_sel:WORD_1
	v_cvt_f32_f16_e32 v136, v158
	v_cvt_f32_f16_e32 v142, v159
	v_fma_mixhi_f16 v169, v193, v173, 0 op_sel:[0,1,0] op_sel_hi:[0,1,0]
	ds_write_b128 v147, v[166:169] offset:2064
	ds_write_b128 v147, v[162:165] offset:8208
	v_mul_f32_e32 v148, v190, v136
	v_mul_f32_e32 v149, v191, v137
	v_mov_b32_e32 v136, v137
	v_mov_b32_e32 v137, v142
	v_cvt_pk_f16_f32 v162, v148, v149
	v_mul_f32_e32 v136, v186, v136
	v_mul_f32_e32 v137, v187, v137
	v_mul_f32_e32 v148, v184, v142
	v_mul_f32_e32 v149, v185, v143
	v_cvt_pk_f16_f32 v159, v136, v137
	v_cvt_f32_f16_sdwa v137, v160 dst_sel:DWORD dst_unused:UNUSED_PAD src0_sel:WORD_1
	v_cvt_f32_f16_e32 v136, v160
	v_cvt_pk_f16_f32 v163, v148, v149
	v_fma_mixlo_f16 v158, v192, v158, 0 op_sel_hi:[0,1,0]
	v_lshlrev_b32_e32 v213, 4, v212
	v_mov_b32_e32 v142, v143
	v_mov_b32_e32 v143, v136
	v_mul_f32_e32 v140, v140, v136
	v_mul_f32_e32 v141, v141, v137
	v_mul_f32_e32 v142, v152, v142
	v_mul_f32_e32 v143, v153, v143
	v_cvt_pk_f16_f32 v164, v140, v141
	v_cvt_pk_f16_f32 v148, v142, v143
	v_cvt_f32_f16_sdwa v143, v161 dst_sel:DWORD dst_unused:UNUSED_PAD src0_sel:WORD_1
	v_cvt_f32_f16_e32 v142, v161
	s_waitcnt vmcnt(0)
	v_cvt_f32_f16_sdwa v141, v157 dst_sel:DWORD dst_unused:UNUSED_PAD src0_sel:WORD_1
	v_cvt_f32_f16_e32 v140, v157
	v_pack_b32_f16 v166, v158, v159
	v_mov_b32_e32 v136, v137
	v_mov_b32_e32 v137, v142
	v_alignbit_b32 v167, v148, v159, 16
	v_mul_f32_e32 v132, v132, v136
	v_mul_f32_e32 v133, v133, v137
	v_cvt_f32_f16_sdwa v137, v155 dst_sel:DWORD dst_unused:UNUSED_PAD src0_sel:WORD_1
	v_cvt_pk_f16_f32 v132, v132, v133
	v_alignbit_b32 v168, v132, v148, 16
	v_lshrrev_b32_e32 v169, 16, v132
	v_mul_f32_e32 v132, v138, v142
	v_mul_f32_e32 v133, v139, v143
	v_cvt_f32_f16_e32 v136, v155
	v_cvt_pk_f16_f32 v165, v132, v133
	v_cvt_f32_f16_sdwa v133, v154 dst_sel:DWORD dst_unused:UNUSED_PAD src0_sel:WORD_1
	v_cvt_f32_f16_e32 v132, v154
	v_cvt_f32_f16_sdwa v139, v156 dst_sel:DWORD dst_unused:UNUSED_PAD src0_sel:WORD_1
	v_cvt_f32_f16_e32 v138, v156
	v_mul_f32_e32 v136, v150, v136
	v_mul_f32_e32 v137, v151, v137
	v_mul_f32_e32 v132, v188, v132
	v_mul_f32_e32 v133, v189, v133
	v_mul_f32_e32 v130, v130, v140
	v_mul_f32_e32 v131, v131, v141
	v_mul_f32_e32 v134, v134, v138
	v_mul_f32_e32 v135, v135, v139
	v_fma_mixhi_f16 v169, v193, v161, 0 op_sel:[0,1,0] op_sel_hi:[0,1,0]
	v_cvt_pk_f16_f32 v132, v132, v133
	v_cvt_pk_f16_f32 v133, v136, v137
	v_cvt_pk_f16_f32 v134, v134, v135
	v_cvt_pk_f16_f32 v135, v130, v131
	v_and_b32_e32 v130, 0xfffffe00, v213
	v_and_b32_e32 v131, 16, v212
	ds_write_b128 v147, v[166:169] offset:4112
	ds_write_b128 v147, v[162:165] offset:10256
	ds_write_b128 v147, v[132:135] offset:6160
	v_or3_b32 v130, v130, v131, v180
	s_waitcnt lgkmcnt(0)
	v_add_u32_e32 v142, s36, v130
	ds_read_b128 v[130:133], v142
	ds_read_b128 v[134:137], v142 offset:2048
	ds_read_b128 v[138:141], v142 offset:1024
	ds_read_b128 v[148:151], v142 offset:3072
	ds_read_b128 v[156:159], v142 offset:4096
	ds_read_b128 v[160:163], v142 offset:5120
	ds_read_b128 v[164:167], v142 offset:6144
	ds_read_b128 v[168:171], v142 offset:7168
	s_waitcnt lgkmcnt(6)
	v_mfma_f32_16x16x32_f16 v[152:155], v[130:133], v[134:137], 0
	v_lshlrev_b32_e32 v208, 2, v179
	v_lshl_add_u32 v215, v144, 2, s36
	v_cmp_gt_i32_e32 vcc, v208, v144
	s_waitcnt lgkmcnt(3)
	v_mfma_f32_16x16x32_f16 v[130:133], v[130:133], v[156:159], 0
	v_lshl_add_u32 v143, v179, 8, v215
	v_or_b32_e32 v211, 1, v208
	v_or_b32_e32 v209, 2, v208
	s_waitcnt lgkmcnt(1)
	v_mfma_f32_16x16x32_f16 v[134:137], v[164:167], v[134:137], 0
	v_or_b32_e32 v210, 3, v208
	v_mfma_f32_16x16x32_f16 v[156:159], v[164:167], v[156:159], 0
	v_mfma_f32_16x16x32_f16 v[130:133], v[138:141], v[160:163], v[130:133]
	v_mfma_f32_16x16x32_f16 v[152:155], v[138:141], v[148:151], v[152:155]
	s_waitcnt lgkmcnt(0)
	v_mfma_f32_16x16x32_f16 v[134:137], v[168:171], v[148:151], v[134:137]
	s_nop 4
	v_cvt_f16_f32_e32 v130, v130
	v_cvt_f16_f32_e32 v131, v131
	v_cndmask_b32_e32 v142, 0, v152, vcc
	v_mfma_f32_16x16x32_f16 v[138:141], v[168:171], v[160:163], v[156:159]
	v_cndmask_b32_e32 v130, 0, v130, vcc
	v_cvt_f16_f32_e32 v134, v134
	v_cvt_f16_f32_e32 v135, v135
	v_cmp_lt_i32_e32 vcc, v208, v144
	ds_write_b32 v143, v142 offset:14336
	s_nop 2
	v_cvt_f16_f32_e32 v138, v138
	v_cvt_f16_f32_e32 v139, v139
	v_cndmask_b32_e64 v142, v153, 0, vcc
	v_lshl_add_u32 v143, v211, 6, v215
	v_cndmask_b32_e64 v134, v134, 0, vcc
	v_cndmask_b32_e64 v138, v138, 0, vcc
	ds_write_b32 v143, v142 offset:14336
	v_cndmask_b32_e64 v142, v131, 0, vcc
	v_cmp_lt_i32_e32 vcc, v211, v144
	v_lshl_add_u32 v143, v209, 6, v215
	v_cvt_f16_f32_e32 v132, v132
	v_cndmask_b32_e64 v135, v135, 0, vcc
	v_cndmask_b32_e64 v139, v139, 0, vcc
	v_cmp_gt_i32_e32 vcc, v209, v144
	v_add_u32_e32 v161, s36, v180
	v_pack_b32_f16 v130, v130, v142
	v_cndmask_b32_e32 v131, 0, v154, vcc
	ds_write_b32 v143, v131 offset:14336
	v_cvt_f16_f32_e32 v131, v136
	v_cvt_f16_f32_e32 v136, v140
	v_cndmask_b32_e32 v132, 0, v132, vcc
	v_cmp_lt_i32_e32 vcc, v209, v144
	v_lshl_add_u32 v143, v210, 6, v215
	s_nop 0
	v_cndmask_b32_e64 v140, v131, 0, vcc
	v_cvt_f16_f32_e32 v131, v133
	v_cndmask_b32_e64 v136, v136, 0, vcc
	v_cmp_gt_i32_e32 vcc, v210, v144
	s_nop 1
	v_cndmask_b32_e32 v131, 0, v131, vcc
	v_pack_b32_f16 v131, v132, v131
	v_cvt_f16_f32_e32 v132, v137
	v_cvt_f16_f32_e32 v137, v141
	v_cndmask_b32_e32 v133, 0, v155, vcc
	v_cmp_lt_i32_e32 vcc, v210, v144
	ds_write_b32 v143, v133 offset:14336
	s_nop 0
	v_cndmask_b32_e64 v132, v132, 0, vcc
	v_pack_b32_f16 v133, v140, v132
	v_pack_b32_f16 v132, v134, v135
	v_cndmask_b32_e64 v134, v137, 0, vcc
	v_pack_b32_f16 v135, v136, v134
	v_lshlrev_b32_e32 v136, 3, v179
	v_add_u32_e32 v160, v161, v136
	v_pack_b32_f16 v134, v138, v139
	ds_write_b64 v160, v[130:131] offset:15872
	ds_write2st64_b64 v160, v[132:133], v[134:135] offset0:4 offset1:5
	s_waitcnt lgkmcnt(0)
	v_cmp_gt_u32_e32 vcc, 16, v212
	s_and_saveexec_b64 s[0:1], vcc
	s_cbranch_execz .LBB0_1289
	v_mov_b32_e32 v179, s36
	v_add_u32_e32 v214, 0x3800, v179
	ds_read2_b64 v[150:153], v214 offset0:8 offset1:16
	ds_read_b128 v[130:133], v179 offset:14528
	ds_read_b128 v[154:157], v179 offset:14592
	v_cmp_eq_u32_e32 vcc, 0, v144
	s_waitcnt lgkmcnt(2)
	v_mov_b32_e32 v136, v152
	v_cndmask_b32_e64 v148, 0, 1.0, vcc
	v_cmp_eq_u32_e32 vcc, 3, v144
	v_mov_b32_e32 v137, v150
	s_waitcnt lgkmcnt(1)
	v_mov_b32_e32 v158, v131
	v_cndmask_b32_e64 v133, 0, 1.0, vcc
	v_cmp_eq_u32_e32 vcc, 1, v144
	v_fma_f32 v147, -v148, v130, v133
	v_mov_b32_e32 v159, v132
	v_cndmask_b32_e64 v135, 0, 1.0, vcc
	v_cmp_eq_u32_e32 vcc, 2, v144
	s_waitcnt lgkmcnt(0)
	v_mov_b32_e32 v175, v154
	v_mov_b32_e32 v205, v156
	v_cndmask_b32_e64 v134, 0, 1.0, vcc
	v_fma_f32 v150, -v148, v136, v134
	v_fma_f32 v151, -v148, v137, v135
	ds_read_b128 v[140:143], v179 offset:15296
	ds_read_b128 v[136:139], v179 offset:15312
	ds_read_b128 v[162:165], v179 offset:14656
	ds_read_b128 v[130:133], v179 offset:14720
	ds_read_b128 v[166:169], v179 offset:14784
	ds_read_b128 v[170:173], v179 offset:14800
	v_cmp_eq_u32_e32 vcc, 4, v144
	s_waitcnt lgkmcnt(3)
	v_mov_b32_e32 v207, v164
	s_waitcnt lgkmcnt(2)
	v_mov_b32_e32 v206, v132
	v_cndmask_b32_e64 v135, 0, 1.0, vcc
	v_cmp_eq_u32_e32 vcc, 7, v144
	s_waitcnt lgkmcnt(1)
	v_mov_b32_e32 v174, v166
	v_mov_b32_e32 v154, v167
	v_cndmask_b32_e64 v134, 0, 1.0, vcc
	v_fma_f32 v134, -v148, v174, v134
	v_fma_f32 v135, -v148, v175, v135
	v_mov_b32_e32 v204, v168
	v_mov_b32_e32 v156, v169
	v_cmp_eq_u32_e32 vcc, 5, v144
	ds_read2_b64 v[166:169], v214 offset0:42 offset1:50
	v_fma_f32 v176, -v151, v154, v134
	v_fma_f32 v177, -v151, v155, v135
	v_cndmask_b32_e64 v135, 0, 1.0, vcc
	v_cmp_eq_u32_e32 vcc, 6, v144
	v_mov_b32_e32 v154, v130
	v_mov_b32_e32 v155, v162
	v_mov_b32_e32 v162, v131
	v_mov_b32_e32 v164, v133
	s_waitcnt lgkmcnt(0)
	v_mov_b32_e32 v167, v172
	ds_read_b128 v[172:175], v179 offset:14848
	ds_read_b128 v[180:183], v179 offset:14864
	ds_read_b128 v[130:133], v179 offset:14944
	ds_read_b128 v[184:187], v179 offset:14976
	ds_read_b128 v[188:191], v179 offset:14912
	ds_read_b128 v[192:195], v179 offset:14928
	v_cndmask_b32_e64 v134, 0, 1.0, vcc
	v_fma_f32 v134, -v148, v154, v134
	v_fma_f32 v135, -v148, v155, v135
	v_cmp_eq_u32_e32 vcc, 10, v144
	v_mov_b32_e32 v149, v151
	ds_read_b128 v[196:199], v179 offset:14992
	ds_read_b128 v[200:203], v179 offset:15040
	s_waitcnt lgkmcnt(5)
	v_cndmask_b32_e64 v131, 0, 1.0, vcc
	s_waitcnt lgkmcnt(4)
	v_mul_f32_e32 v132, v148, v184
	v_mul_f32_e32 v133, v149, v185
	v_fma_f32 v162, -v151, v162, v134
	v_fma_f32 v163, -v151, v163, v135
	v_sub_f32_e32 v131, v131, v132
	v_sub_f32_e32 v131, v131, v133
	ds_read2_b64 v[132:135], v214 offset0:84 offset1:110
	v_cmp_eq_u32_e32 vcc, 11, v144
	v_mov_b32_e32 v152, v151
	s_waitcnt lgkmcnt(1)
	v_mov_b32_e32 v184, v201
	s_waitcnt lgkmcnt(0)
	v_cndmask_b32_e64 v135, 0, 1.0, vcc
	v_fma_f32 v154, -v148, v200, v135
	v_mov_b32_e32 v185, v151
	v_mov_b32_e32 v155, v150
	v_fma_f32 v152, -v152, v184, v154
	v_fma_f32 v153, -v153, v185, v155
	v_mov_b32_e32 v154, v151
	v_mov_b32_e32 v155, v153
	v_mul_f32_e32 v154, v158, v154
	v_mul_f32_e32 v155, v159, v155
	v_fma_f32 v158, -v153, v204, v176
	v_fma_f32 v159, -v153, v205, v177
	v_sub_f32_e32 v135, v147, v154
	v_sub_f32_e32 v154, v135, v155
	v_fma_f32 v156, -v154, v156, v158
	v_fma_f32 v157, -v154, v157, v159
	v_fma_f32 v158, -v153, v206, v162
	v_fma_f32 v159, -v153, v207, v163
	v_mov_b32_e32 v162, v153
	v_mov_b32_e32 v163, v154
	v_mov_b32_e32 v216, v168
	v_mov_b32_e32 v217, v166
	v_fma_f32 v158, -v154, v164, v158
	v_fma_f32 v159, -v154, v165, v159
	v_mul_f32_e32 v162, v162, v186
	v_mul_f32_e32 v163, v163, v187
	v_fma_f32 v158, -v216, v157, v158
	v_fma_f32 v159, -v217, v157, v159
	v_sub_f32_e32 v131, v131, v162
	v_sub_f32_e32 v131, v131, v163
	v_mov_b32_e32 v162, v157
	v_mov_b32_e32 v163, v159
	v_mul_f32_e32 v162, v162, v196
	v_mul_f32_e32 v163, v163, v197
	v_mov_b32_e32 v166, v171
	v_sub_f32_e32 v131, v131, v162
	v_sub_f32_e32 v131, v131, v163
	ds_read_b128 v[162:165], v179 offset:15056
	ds_read_b128 v[184:187], v179 offset:15072
	v_fma_f32 v135, -v157, v170, v156
	v_mov_b32_e32 v155, v157
	v_mov_b32_e32 v170, v203
	s_waitcnt lgkmcnt(1)
	v_mov_b32_e32 v171, v162
	v_fma_f32 v147, -v153, v202, v152
	v_mul_f32_e32 v170, v154, v170
	v_mul_f32_e32 v171, v155, v171
	v_mov_b32_e32 v168, v159
	v_sub_f32_e32 v147, v147, v170
	v_sub_f32_e32 v162, v147, v171
	v_mov_b32_e32 v170, v163
	v_mov_b32_e32 v171, v159
	v_mov_b32_e32 v163, v158
	v_fma_f32 v196, -v168, v170, v162
	v_fma_f32 v197, -v169, v171, v163
	v_mov_b32_e32 v162, v159
	v_mov_b32_e32 v163, v197
	v_mul_f32_e32 v162, v166, v162
	v_mul_f32_e32 v163, v167, v163
	v_mov_b32_e32 v200, v197
	v_sub_f32_e32 v135, v135, v162
	v_sub_f32_e32 v201, v135, v163
	v_mul_f32_e32 v162, v200, v198
	v_mul_f32_e32 v163, v201, v199
	v_cmp_eq_u32_e32 vcc, 8, v144
	v_sub_f32_e32 v131, v131, v162
	v_sub_f32_e32 v131, v131, v163
	v_cndmask_b32_e64 v163, 0, 1.0, vcc
	v_cmp_eq_u32_e32 vcc, 9, v144
	v_mov_b32_e32 v166, v188
	v_mov_b32_e32 v167, v172
	v_cndmask_b32_e64 v162, 0, 1.0, vcc
	v_fma_f32 v162, -v148, v166, v162
	v_fma_f32 v163, -v148, v167, v163
	v_mov_b32_e32 v172, v189
	v_fma_f32 v162, -v151, v172, v162
	v_fma_f32 v163, -v151, v173, v163
	v_mov_b32_e32 v166, v190
	v_mov_b32_e32 v167, v174
	v_fma_f32 v162, -v153, v166, v162
	v_fma_f32 v163, -v153, v167, v163
	v_mov_b32_e32 v174, v191
	v_fma_f32 v162, -v154, v174, v162
	v_fma_f32 v163, -v154, v175, v163
	v_mov_b32_e32 v166, v192
	v_mov_b32_e32 v167, v180
	v_fma_f32 v162, -v157, v166, v162
	v_fma_f32 v163, -v157, v167, v163
	v_mov_b32_e32 v180, v193
	v_fma_f32 v162, -v159, v180, v162
	v_fma_f32 v163, -v159, v181, v163
	v_mov_b32_e32 v166, v194
	v_mov_b32_e32 v167, v182
	v_fma_f32 v162, -v197, v166, v162
	v_fma_f32 v163, -v197, v167, v163
	v_mov_b32_e32 v182, v195
	v_mov_b32_e32 v188, v201
	v_fma_f32 v190, -v182, v188, v162
	v_fma_f32 v191, -v183, v188, v163
	v_fma_f32 v135, -v197, v164, v196
	v_fma_f32 v193, -v130, v191, v190
	v_mov_b32_e32 v192, v191
	v_mov_b32_e32 v162, v201
	v_mov_b32_e32 v163, v191
	v_mov_b32_e32 v164, v165
	s_waitcnt lgkmcnt(0)
	v_mov_b32_e32 v165, v184
	v_mul_f32_e32 v132, v132, v192
	v_mul_f32_e32 v133, v133, v193
	v_mul_f32_e32 v162, v162, v164
	v_mul_f32_e32 v163, v163, v165
	v_sub_f32_e32 v131, v131, v132
	v_sub_f32_e32 v132, v135, v162
	v_sub_f32_e32 v135, v132, v163
	v_sub_f32_e32 v133, v131, v133
	v_mov_b32_e32 v162, v185
	v_mov_b32_e32 v163, v186
	v_mov_b32_e32 v132, v193
	v_mul_f32_e32 v162, v162, v132
	v_mul_f32_e32 v163, v163, v133
	v_cmp_eq_u32_e32 vcc, 12, v144
	v_sub_f32_e32 v131, v135, v162
	v_sub_f32_e32 v192, v131, v163
	ds_read_b128 v[162:165], v179 offset:15328
	ds_read_b128 v[166:169], v179 offset:15344
	ds_read_b128 v[170:173], v179 offset:15104
	ds_read_b128 v[174:177], v179 offset:15120
	ds_read_b128 v[180:183], v179 offset:15136
	v_cndmask_b32_e64 v147, 0, 1.0, vcc
	v_mov_b32_e32 v184, v140
	s_waitcnt lgkmcnt(2)
	v_mov_b32_e32 v185, v170
	v_fma_f32 v146, -v148, v184, v146
	v_fma_f32 v147, -v148, v185, v147
	v_mov_b32_e32 v170, v141
	v_fma_f32 v140, -v151, v170, v146
	v_fma_f32 v141, -v151, v171, v147
	v_mov_b32_e32 v146, v142
	v_mov_b32_e32 v147, v172
	v_fma_f32 v140, -v146, v153, v140
	v_fma_f32 v141, -v147, v153, v141
	v_mov_b32_e32 v172, v143
	v_fma_f32 v140, -v172, v154, v140
	v_fma_f32 v141, -v173, v154, v141
	v_mov_b32_e32 v142, v136
	s_waitcnt lgkmcnt(1)
	v_mov_b32_e32 v143, v174
	v_fma_f32 v140, -v157, v142, v140
	v_fma_f32 v141, -v157, v143, v141
	v_mov_b32_e32 v174, v137
	v_fma_f32 v136, -v159, v174, v140
	v_fma_f32 v137, -v159, v175, v141
	v_mov_b32_e32 v140, v138
	v_mov_b32_e32 v141, v176
	v_fma_f32 v136, -v140, v197, v136
	v_fma_f32 v137, -v141, v197, v137
	v_mov_b32_e32 v176, v139
	v_fma_f32 v140, -v176, v188, v136
	v_fma_f32 v141, -v177, v188, v137
	v_mov_b32_e32 v142, v162
	s_waitcnt lgkmcnt(0)
	v_mov_b32_e32 v143, v180
	v_fma_f32 v140, -v142, v191, v140
	v_fma_f32 v141, -v143, v191, v141
	v_mov_b32_e32 v180, v163
	v_fma_f32 v140, -v180, v132, v140
	v_fma_f32 v141, -v181, v132, v141
	v_mov_b32_e32 v142, v164
	v_mov_b32_e32 v143, v182
	v_mov_b32_e32 v146, v133
	v_fma_f32 v140, -v142, v146, v140
	v_fma_f32 v141, -v143, v146, v141
	v_mov_b32_e32 v182, v165
	ds_read_b128 v[136:139], v179 offset:15168
	v_fma_f32 v194, -v182, v192, v140
	v_fma_f32 v195, -v183, v192, v141
	ds_read_b128 v[140:143], v179 offset:15184
	ds_read_b128 v[162:165], v179 offset:15200
	ds_read_b128 v[170:173], v179 offset:15232
	v_cmp_eq_u32_e32 vcc, 13, v144
	ds_read_b128 v[174:177], v179 offset:15248
	s_waitcnt lgkmcnt(4)
	v_mov_b32_e32 v183, v136
	v_cndmask_b32_e64 v181, 0, 1.0, vcc
	v_cmp_eq_u32_e32 vcc, 14, v144
	s_waitcnt lgkmcnt(1)
	v_mov_b32_e32 v182, v170
	v_mov_b32_e32 v136, v171
	v_cndmask_b32_e64 v180, 0, 1.0, vcc
	v_fma_f32 v198, -v148, v182, v180
	v_fma_f32 v199, -v148, v183, v181
	v_fma_f32 v136, -v151, v136, v198
	v_fma_f32 v137, -v151, v137, v199
	v_mov_b32_e32 v170, v172
	v_mov_b32_e32 v171, v138
	v_fma_f32 v136, -v153, v170, v136
	v_fma_f32 v137, -v153, v171, v137
	v_mov_b32_e32 v138, v173
	ds_read_b128 v[180:183], v179 offset:15264
	ds_read_b128 v[184:187], v179 offset:15280
	v_fma_f32 v136, -v154, v138, v136
	v_fma_f32 v137, -v154, v139, v137
	s_waitcnt lgkmcnt(2)
	v_mov_b32_e32 v138, v174
	v_mov_b32_e32 v139, v140
	v_fma_f32 v136, -v157, v138, v136
	v_fma_f32 v137, -v157, v139, v137
	v_mov_b32_e32 v140, v175
	v_fma_f32 v136, -v159, v140, v136
	v_fma_f32 v137, -v159, v141, v137
	v_mov_b32_e32 v138, v176
	v_mov_b32_e32 v139, v142
	v_fma_f32 v136, -v197, v138, v136
	v_fma_f32 v137, -v197, v139, v137
	v_mov_b32_e32 v142, v177
	v_fma_f32 v136, -v188, v142, v136
	v_fma_f32 v137, -v188, v143, v137
	s_waitcnt lgkmcnt(1)
	v_mov_b32_e32 v138, v180
	v_mov_b32_e32 v139, v162
	v_fma_f32 v136, -v191, v138, v136
	v_fma_f32 v137, -v191, v139, v137
	v_mov_b32_e32 v162, v181
	v_fma_f32 v136, -v132, v162, v136
	v_fma_f32 v137, -v132, v163, v137
	v_mov_b32_e32 v138, v182
	v_mov_b32_e32 v139, v164
	v_fma_f32 v136, -v146, v138, v136
	v_fma_f32 v137, -v146, v139, v137
	v_mov_b32_e32 v164, v183
	v_fma_f32 v136, -v192, v164, v136
	v_fma_f32 v137, -v192, v165, v137
	s_waitcnt lgkmcnt(0)
	v_mov_b32_e32 v138, v184
	v_mov_b32_e32 v139, v134
	v_fma_f32 v136, -v138, v195, v136
	v_fma_f32 v137, -v139, v195, v137
	v_mov_b32_e32 v138, v167
	v_fma_f32 v135, -v185, v137, v136
	v_mov_b32_e32 v139, v168
	v_mov_b32_e32 v134, v137
	v_cvt_f16_f32_e32 v132, v191
	v_fma_f32 v131, -v166, v195, v194
	v_mul_f32_e32 v138, v138, v134
	v_mul_f32_e32 v139, v139, v135
	v_cvt_pk_f16_f32 v134, v195, v137
	v_sub_f32_e32 v131, v131, v138
	v_sub_f32_e32 v131, v131, v139
	v_cvt_pk_f16_f32 v139, v197, v201
	v_cvt_pk_f16_f32 v138, v157, v159
	v_cvt_pk_f16_f32 v137, v153, v154
	v_cvt_pk_f16_f32 v136, v148, v151
	v_cvt_pk_f16_f32 v135, v135, v131
	v_cvt_pk_f16_f32 v133, v133, v192
	v_fma_mixhi_f16 v132, -v130, v191, v190
	ds_write_b128 v161, v[136:139] offset:15360
	ds_write_b128 v161, v[132:135] offset:15376
	s_branch .LBB0_1289
